# placement pin: heads of the ten GEMM K-loops, the attention tile loop and the conv tap loop aligned to 64 bytes (.p2align 6 in front of the loop label; pad nops run once per loop entry)
# speedup vs baseline: 1.0042x; 1.0015x over previous
.LBB0_134:
	s_ashr_i32 s25, s24, 31
	s_lshl_b64 s[4:5], s[24:25], 18
	s_add_u32 s26, s36, s4
	s_addc_u32 s27, s37, s5
	s_and_b64 s[4:5], s[6:7], exec
	s_cselect_b32 s25, s27, s31
	s_cselect_b32 s45, s26, s30
	s_ashr_i32 s23, s22, 31
	s_lshl_b64 s[4:5], s[22:23], 18
	s_add_u32 s28, s40, s4
	s_addc_u32 s29, s41, s5
	s_and_b64 s[4:5], s[6:7], exec
	s_cselect_b32 s23, s29, s9
	s_cselect_b32 s80, s28, s8
	s_add_i32 s34, 0, 0x10000
	s_add_i32 s90, 0, 0x14000
	v_add_u32_e32 v130, s34, v192
	v_add_u32_e32 v131, s90, v192
	ds_read_b128 v[2:5], v130
	ds_read_b128 v[6:9], v130 offset:1024
	ds_read_b128 v[10:13], v130 offset:2048
	ds_read_b128 v[14:17], v130 offset:3072
	ds_read_b128 v[18:21], v131
	ds_read_b128 v[22:25], v131 offset:1024
	ds_read_b128 v[26:29], v131 offset:2048
	ds_read_b128 v[30:33], v131 offset:3072
	s_add_u32 s4, s30, 0x20080
	s_addc_u32 s5, s31, 0
	s_add_i32 s88, s52, 0xc000
	v_lshl_add_u64 v[66:67], s[4:5], 0, v[150:151]
	s_mov_b32 m0, s88
	s_add_i32 s89, s52, 0xe000
	ds_read_b128 v[34:37], v193
	ds_read_b128 v[38:41], v193 offset:1024
	ds_read_b128 v[42:45], v193 offset:2048
	ds_read_b128 v[46:49], v193 offset:3072
	ds_read_b128 v[50:53], v193 offset:4096
	ds_read_b128 v[54:57], v193 offset:5120
	ds_read_b128 v[58:61], v193 offset:6144
	ds_read_b128 v[62:65], v193 offset:7168
	global_load_lds_dwordx4 v[66:67], off
	v_lshl_add_u64 v[66:67], s[4:5], 0, v[148:149]
	s_mov_b32 m0, s89
	s_nop 0
	global_load_lds_dwordx4 v[66:67], off
	s_waitcnt vmcnt(8)
	s_waitcnt lgkmcnt(0)
	s_barrier
	s_setprio 1
	s_waitcnt lgkmcnt(0)
	v_mfma_i32_16x16x64_i8 v[90:93], v[2:5], v[58:61], 0
	s_mov_b32 vcc_lo, 0
	v_mfma_i32_16x16x64_i8 v[66:69], v[2:5], v[34:37], 0
	v_mfma_i32_16x16x64_i8 v[70:73], v[10:13], v[34:37], 0
	v_mfma_i32_16x16x64_i8 v[74:77], v[2:5], v[42:45], 0
	v_mfma_i32_16x16x64_i8 v[78:81], v[10:13], v[42:45], 0
	v_mfma_i32_16x16x64_i8 v[82:85], v[2:5], v[50:53], 0
	v_mfma_i32_16x16x64_i8 v[86:89], v[10:13], v[50:53], 0
	v_mfma_i32_16x16x64_i8 v[94:97], v[6:9], v[62:65], v[90:93]
	v_mfma_i32_16x16x64_i8 v[90:93], v[10:13], v[58:61], 0
	v_mfma_i32_16x16x64_i8 v[66:69], v[6:9], v[38:41], v[66:69]
	v_mfma_i32_16x16x64_i8 v[70:73], v[14:17], v[38:41], v[70:73]
	v_mfma_i32_16x16x64_i8 v[74:77], v[6:9], v[46:49], v[74:77]
	v_mfma_i32_16x16x64_i8 v[78:81], v[14:17], v[46:49], v[78:81]
	v_mfma_i32_16x16x64_i8 v[82:85], v[6:9], v[54:57], v[82:85]
	v_mfma_i32_16x16x64_i8 v[86:89], v[14:17], v[54:57], v[86:89]
	v_mfma_i32_16x16x64_i8 v[102:105], v[14:17], v[62:65], v[90:93]
	s_setprio 0
	s_setprio 1
	v_mfma_i32_16x16x64_i8 v[90:93], v[18:21], v[34:37], 0
	v_mfma_i32_16x16x64_i8 v[34:37], v[26:29], v[34:37], 0
	v_mfma_i32_16x16x64_i8 v[110:113], v[22:25], v[38:41], v[90:93]
	v_mfma_i32_16x16x64_i8 v[34:37], v[30:33], v[38:41], v[34:37]
	v_mfma_i32_16x16x64_i8 v[38:41], v[18:21], v[42:45], 0
	v_mfma_i32_16x16x64_i8 v[42:45], v[26:29], v[42:45], 0
	v_mfma_i32_16x16x64_i8 v[38:41], v[22:25], v[46:49], v[38:41]
	v_mfma_i32_16x16x64_i8 v[42:45], v[30:33], v[46:49], v[42:45]
	v_mfma_i32_16x16x64_i8 v[46:49], v[18:21], v[50:53], 0
	v_mfma_i32_16x16x64_i8 v[50:53], v[26:29], v[50:53], 0
	v_mfma_i32_16x16x64_i8 v[46:49], v[22:25], v[54:57], v[46:49]
	v_mfma_i32_16x16x64_i8 v[50:53], v[30:33], v[54:57], v[50:53]
	v_mfma_i32_16x16x64_i8 v[54:57], v[18:21], v[58:61], 0
	v_mfma_i32_16x16x64_i8 v[58:61], v[26:29], v[58:61], 0
	v_mfma_i32_16x16x64_i8 v[54:57], v[22:25], v[62:65], v[54:57]
	v_mfma_i32_16x16x64_i8 v[58:61], v[30:33], v[62:65], v[58:61]
	s_setprio 0
	s_barrier
	s_add_i32 s4, s34, s49
	v_lshl_add_u64 v[230:231], s[8:9], 0, v[0:1]
	s_add_i32 s5, s4, 0x2000
	v_lshl_add_u64 v[132:133], v[230:231], 0, s[92:93]
	s_mov_b32 m0, s4
	v_lshl_add_u64 v[244:245], s[8:9], 0, v[146:147]
	s_add_u32 s34, s8, 0x20100
	ds_read_b128 v[62:65], v193 offset:16384
	ds_read_b128 v[90:93], v193 offset:17408
	ds_read_b128 v[98:101], v193 offset:18432
	ds_read_b128 v[106:109], v193 offset:19456
	ds_read_b128 v[114:117], v193 offset:20480
	ds_read_b128 v[118:121], v193 offset:21504
	ds_read_b128 v[122:125], v193 offset:22528
	ds_read_b128 v[126:129], v193 offset:23552
	global_load_lds_dwordx4 v[132:133], off
	v_lshl_add_u64 v[132:133], v[244:245], 0, s[92:93]
	s_mov_b32 m0, s5
	s_addc_u32 s35, s9, 0
	s_add_i32 s90, s90, s49
	global_load_lds_dwordx4 v[132:133], off
	v_lshl_add_u64 v[132:133], s[34:35], 0, v[0:1]
	s_mov_b32 m0, s90
	s_add_i32 vcc_hi, s90, 0x2000
	global_load_lds_dwordx4 v[132:133], off
	v_lshl_add_u64 v[132:133], s[34:35], 0, v[146:147]
	s_mov_b32 m0, vcc_hi
	v_lshl_add_u64 v[246:247], s[30:31], 0, v[150:151]
	global_load_lds_dwordx4 v[132:133], off
	v_lshl_add_u64 v[132:133], v[246:247], 0, s[92:93]
	s_mov_b32 m0, s52
	v_lshl_add_u64 v[232:233], s[30:31], 0, v[148:149]
	global_load_lds_dwordx4 v[132:133], off
	v_lshl_add_u64 v[132:133], v[232:233], 0, s[92:93]
	s_mov_b32 m0, s70
	s_nop 0
	global_load_lds_dwordx4 v[132:133], off
	s_waitcnt vmcnt(8)
	s_waitcnt lgkmcnt(0)
	s_barrier
	s_setprio 1
	s_waitcnt lgkmcnt(0)
	v_mfma_i32_16x16x64_i8 v[132:135], v[2:5], v[62:65], 0
	v_mfma_i32_16x16x64_i8 v[142:145], v[2:5], v[98:101], 0
	v_mfma_i32_16x16x64_i8 v[160:163], v[2:5], v[114:117], 0
	v_mfma_i32_16x16x64_i8 v[2:5], v[2:5], v[122:125], 0
	v_mfma_i32_16x16x64_i8 v[134:137], v[6:9], v[90:93], v[132:135]
	v_mfma_i32_16x16x64_i8 v[142:145], v[6:9], v[106:109], v[142:145]
	v_mfma_i32_16x16x64_i8 v[160:163], v[6:9], v[118:121], v[160:163]
	v_mfma_i32_16x16x64_i8 v[2:5], v[6:9], v[126:129], v[2:5]
	v_mfma_i32_16x16x64_i8 v[6:9], v[10:13], v[122:125], 0
	v_mfma_i32_16x16x64_i8 v[138:141], v[10:13], v[62:65], 0
	v_mfma_i32_16x16x64_i8 v[156:159], v[10:13], v[98:101], 0
	v_mfma_i32_16x16x64_i8 v[164:167], v[10:13], v[114:117], 0
	v_mfma_i32_16x16x64_i8 v[6:9], v[14:17], v[126:129], v[6:9]
	v_mfma_i32_16x16x64_i8 v[138:141], v[14:17], v[90:93], v[138:141]
	v_mfma_i32_16x16x64_i8 v[156:159], v[14:17], v[106:109], v[156:159]
	v_mfma_i32_16x16x64_i8 v[164:167], v[14:17], v[118:121], v[164:167]
	s_setprio 0
	s_setprio 1
	v_mfma_i32_16x16x64_i8 v[14:17], v[26:29], v[62:65], 0
	v_mfma_i32_16x16x64_i8 v[168:171], v[30:33], v[90:93], v[14:17]
	v_mfma_i32_16x16x64_i8 v[14:17], v[18:21], v[98:101], 0
	v_mfma_i32_16x16x64_i8 v[172:175], v[22:25], v[106:109], v[14:17]
	v_mfma_i32_16x16x64_i8 v[14:17], v[26:29], v[98:101], 0
	v_mfma_i32_16x16x64_i8 v[176:179], v[30:33], v[106:109], v[14:17]
	v_mfma_i32_16x16x64_i8 v[14:17], v[18:21], v[114:117], 0
	v_mfma_i32_16x16x64_i8 v[180:183], v[22:25], v[118:121], v[14:17]
	v_mfma_i32_16x16x64_i8 v[14:17], v[26:29], v[114:117], 0
	v_mfma_i32_16x16x64_i8 v[10:13], v[18:21], v[62:65], 0
	v_mfma_i32_16x16x64_i8 v[184:187], v[30:33], v[118:121], v[14:17]
	v_mfma_i32_16x16x64_i8 v[14:17], v[18:21], v[122:125], 0
	v_mfma_i32_16x16x64_i8 v[10:13], v[22:25], v[90:93], v[10:13]
	v_mfma_i32_16x16x64_i8 v[188:191], v[22:25], v[126:129], v[14:17]
	v_mfma_i32_16x16x64_i8 v[14:17], v[26:29], v[122:125], 0
	v_mfma_i32_16x16x64_i8 v[198:201], v[30:33], v[126:129], v[14:17]
	s_setprio 0
	s_barrier
	s_add_i32 s50, 0, 0x18000
	s_add_i32 s94, 0, 0x1c000
	v_add_u32_e32 v132, s50, v192
	v_add_u32_e32 v133, s94, v192
	s_nop 0
	ds_read_b128 v[14:17], v132
	ds_read_b128 v[22:25], v132 offset:1024
	ds_read_b128 v[26:29], v132 offset:2048
	ds_read_b128 v[62:65], v132 offset:3072
	ds_read_b128 v[202:205], v133
	ds_read_b128 v[206:209], v133 offset:1024
	ds_read_b128 v[210:213], v133 offset:2048
	ds_read_b128 v[214:217], v133 offset:3072
	s_add_u32 s34, s30, 0x20100
	s_addc_u32 s35, s31, 0
	s_mov_b32 m0, s71
	v_lshl_add_u64 v[90:91], s[34:35], 0, v[150:151]
	ds_read_b128 v[18:21], v193 offset:32768
	ds_read_b128 v[30:33], v193 offset:33792
	ds_read_b128 v[218:221], v193 offset:34816
	ds_read_b128 v[222:225], v193 offset:35840
	ds_read_b128 v[226:229], v193 offset:36864
	ds_read_b128 v[248:251], v193 offset:37888
	ds_read_b128 v[240:243], v193 offset:38912
	ds_read_b128 v[194:197], v193 offset:39936
	global_load_lds_dwordx4 v[90:91], off
	v_lshl_add_u64 v[90:91], s[34:35], 0, v[148:149]
	s_mov_b32 m0, s75
	s_nop 0
	global_load_lds_dwordx4 v[90:91], off
	s_waitcnt vmcnt(8)
	s_waitcnt lgkmcnt(0)
	s_barrier
	s_setprio 1
	s_waitcnt lgkmcnt(0)
	v_mfma_i32_16x16x64_i8 v[66:69], v[14:17], v[18:21], v[66:69]
	v_mfma_i32_16x16x64_i8 v[122:125], v[22:25], v[30:33], v[66:69]
	v_mfma_i32_16x16x64_i8 v[66:69], v[26:29], v[18:21], v[70:73]
	v_mfma_i32_16x16x64_i8 v[114:117], v[62:65], v[30:33], v[66:69]
	v_mfma_i32_16x16x64_i8 v[66:69], v[14:17], v[218:221], v[74:77]
	v_mfma_i32_16x16x64_i8 v[106:109], v[22:25], v[222:225], v[66:69]
	v_mfma_i32_16x16x64_i8 v[66:69], v[26:29], v[218:221], v[78:81]
	v_mfma_i32_16x16x64_i8 v[98:101], v[62:65], v[222:225], v[66:69]
	v_mfma_i32_16x16x64_i8 v[66:69], v[14:17], v[226:229], v[82:85]
	v_mfma_i32_16x16x64_i8 v[90:93], v[22:25], v[248:251], v[66:69]
	v_mfma_i32_16x16x64_i8 v[66:69], v[26:29], v[226:229], v[86:89]
	v_mfma_i32_16x16x64_i8 v[82:85], v[62:65], v[248:251], v[66:69]
	v_mfma_i32_16x16x64_i8 v[66:69], v[14:17], v[240:243], v[94:97]
	v_mfma_i32_16x16x64_i8 v[74:77], v[22:25], v[194:197], v[66:69]
	v_mfma_i32_16x16x64_i8 v[66:69], v[26:29], v[240:243], v[102:105]
	v_mfma_i32_16x16x64_i8 v[66:69], v[62:65], v[194:197], v[66:69]
	s_setprio 0
	s_setprio 1
	v_mfma_i32_16x16x64_i8 v[70:73], v[202:205], v[18:21], v[110:113]
	v_mfma_i32_16x16x64_i8 v[18:21], v[210:213], v[18:21], v[34:37]
	v_mfma_i32_16x16x64_i8 v[118:121], v[214:217], v[30:33], v[18:21]
	v_mfma_i32_16x16x64_i8 v[18:21], v[202:205], v[218:221], v[38:41]
	v_mfma_i32_16x16x64_i8 v[110:113], v[206:209], v[222:225], v[18:21]
	v_mfma_i32_16x16x64_i8 v[18:21], v[210:213], v[218:221], v[42:45]
	v_mfma_i32_16x16x64_i8 v[102:105], v[214:217], v[222:225], v[18:21]
	v_mfma_i32_16x16x64_i8 v[18:21], v[202:205], v[226:229], v[46:49]
	v_mfma_i32_16x16x64_i8 v[94:97], v[206:209], v[248:251], v[18:21]
	v_mfma_i32_16x16x64_i8 v[18:21], v[210:213], v[226:229], v[50:53]
	v_mfma_i32_16x16x64_i8 v[86:89], v[214:217], v[248:251], v[18:21]
	v_mfma_i32_16x16x64_i8 v[18:21], v[202:205], v[240:243], v[54:57]
	v_mfma_i32_16x16x64_i8 v[78:81], v[206:209], v[194:197], v[18:21]
	v_mfma_i32_16x16x64_i8 v[18:21], v[210:213], v[240:243], v[58:61]
	v_mfma_i32_16x16x64_i8 v[126:129], v[206:209], v[30:33], v[70:73]
	v_mfma_i32_16x16x64_i8 v[70:73], v[214:217], v[194:197], v[18:21]
	s_setprio 0
	s_barrier
	s_add_i32 s50, s50, s49
	s_mov_b64 s[54:55], 0x180
	s_add_i32 s51, s50, 0x2000
	s_nop 0
	v_lshl_add_u64 v[18:19], v[230:231], 0, s[54:55]
	s_mov_b32 m0, s50
	s_add_u32 s34, s8, 0x20180
	ds_read_b128 v[38:41], v193 offset:49152
	ds_read_b128 v[46:49], v193 offset:50176
	ds_read_b128 v[194:197], v193 offset:51200
	ds_read_b128 v[218:221], v193 offset:52224
	ds_read_b128 v[222:225], v193 offset:53248
	ds_read_b128 v[226:229], v193 offset:54272
	ds_read_b128 v[240:243], v193 offset:55296
	ds_read_b128 v[248:251], v193 offset:56320
	global_load_lds_dwordx4 v[18:19], off
	v_lshl_add_u64 v[18:19], v[244:245], 0, s[54:55]
	s_mov_b32 m0, s51
	s_addc_u32 s35, s9, 0
	s_add_i32 s94, s94, s49
	global_load_lds_dwordx4 v[18:19], off
	v_lshl_add_u64 v[18:19], s[34:35], 0, v[0:1]
	s_mov_b32 m0, s94
	s_add_i32 s95, s94, 0x2000
	global_load_lds_dwordx4 v[18:19], off
	v_lshl_add_u64 v[18:19], s[34:35], 0, v[146:147]
	s_mov_b32 m0, s95
	s_nop 0
	global_load_lds_dwordx4 v[18:19], off
	v_lshl_add_u64 v[18:19], v[246:247], 0, s[54:55]
	s_mov_b32 m0, s59
	s_nop 0
	global_load_lds_dwordx4 v[18:19], off
	v_lshl_add_u64 v[18:19], v[232:233], 0, s[54:55]
	s_mov_b32 m0, s33
	s_nop 0
	global_load_lds_dwordx4 v[18:19], off
	s_waitcnt vmcnt(8)
	s_waitcnt lgkmcnt(0)
	s_barrier
	s_setprio 1
	s_waitcnt lgkmcnt(0)
	v_mfma_i32_16x16x64_i8 v[18:21], v[14:17], v[38:41], v[134:137]
	v_mfma_i32_16x16x64_i8 v[58:61], v[22:25], v[46:49], v[18:21]
	v_mfma_i32_16x16x64_i8 v[18:21], v[26:29], v[38:41], v[138:141]
	v_mfma_i32_16x16x64_i8 v[50:53], v[62:65], v[46:49], v[18:21]
	v_mfma_i32_16x16x64_i8 v[18:21], v[14:17], v[194:197], v[142:145]
	v_mfma_i32_16x16x64_i8 v[42:45], v[22:25], v[218:221], v[18:21]
	v_mfma_i32_16x16x64_i8 v[18:21], v[26:29], v[194:197], v[156:159]
	v_mfma_i32_16x16x64_i8 v[34:37], v[62:65], v[218:221], v[18:21]
	v_mfma_i32_16x16x64_i8 v[18:21], v[14:17], v[222:225], v[160:163]
	v_mfma_i32_16x16x64_i8 v[2:5], v[14:17], v[240:243], v[2:5]
	v_mfma_i32_16x16x64_i8 v[30:33], v[22:25], v[226:229], v[18:21]
	v_mfma_i32_16x16x64_i8 v[18:21], v[26:29], v[222:225], v[164:167]
	v_mfma_i32_16x16x64_i8 v[14:17], v[22:25], v[248:251], v[2:5]
	v_mfma_i32_16x16x64_i8 v[2:5], v[26:29], v[240:243], v[6:9]
	v_mfma_i32_16x16x64_i8 v[18:21], v[62:65], v[226:229], v[18:21]
	v_mfma_i32_16x16x64_i8 v[2:5], v[62:65], v[248:251], v[2:5]
	s_setprio 0
	s_setprio 1
	v_mfma_i32_16x16x64_i8 v[6:9], v[202:205], v[38:41], v[10:13]
	v_mfma_i32_16x16x64_i8 v[62:65], v[206:209], v[46:49], v[6:9]
	v_mfma_i32_16x16x64_i8 v[6:9], v[210:213], v[38:41], v[168:171]
	v_mfma_i32_16x16x64_i8 v[54:57], v[214:217], v[46:49], v[6:9]
	v_mfma_i32_16x16x64_i8 v[6:9], v[202:205], v[194:197], v[172:175]
	v_mfma_i32_16x16x64_i8 v[46:49], v[206:209], v[218:221], v[6:9]
	v_mfma_i32_16x16x64_i8 v[6:9], v[210:213], v[194:197], v[176:179]
	v_mfma_i32_16x16x64_i8 v[38:41], v[214:217], v[218:221], v[6:9]
	v_mfma_i32_16x16x64_i8 v[6:9], v[202:205], v[222:225], v[180:183]
	v_mfma_i32_16x16x64_i8 v[26:29], v[206:209], v[226:229], v[6:9]
	v_mfma_i32_16x16x64_i8 v[6:9], v[210:213], v[222:225], v[184:187]
	v_mfma_i32_16x16x64_i8 v[22:25], v[214:217], v[226:229], v[6:9]
	v_mfma_i32_16x16x64_i8 v[6:9], v[202:205], v[240:243], v[188:191]
	v_mfma_i32_16x16x64_i8 v[10:13], v[206:209], v[248:251], v[6:9]
	v_mfma_i32_16x16x64_i8 v[6:9], v[210:213], v[240:243], v[198:201]
	v_mfma_i32_16x16x64_i8 v[6:9], v[214:217], v[248:251], v[6:9]
	s_setprio 0
	s_barrier
	s_add_u32 s30, s30, 0x20180
	s_addc_u32 s31, s31, 0
	s_add_u32 s48, s8, 0x200
	s_addc_u32 s58, s9, 0
	.p2align	6

.LBB0_194:
	s_ashr_i32 s21, s20, 31
	s_lshl_b64 s[4:5], s[20:21], 18
	s_add_u32 s22, s33, s4
	s_addc_u32 s23, s34, s5
	s_and_b64 s[4:5], s[6:7], exec
	s_cselect_b32 s21, s23, s27
	s_cselect_b32 s70, s22, s26
	s_ashr_i32 s19, s18, 31
	s_lshl_b64 s[4:5], s[18:19], 18
	s_add_u32 s24, s35, s4
	s_addc_u32 s25, s36, s5
	s_and_b64 s[4:5], s[6:7], exec
	s_cselect_b32 s19, s25, s29
	s_cselect_b32 s71, s24, s28
	s_add_u32 s26, s26, 0x20080
	s_addc_u32 s27, s27, 0
	s_add_u32 s75, s28, 0x100
	v_mov_b32_e32 v2, 0
	s_addc_u32 s80, s29, 0
	s_mov_b32 s88, -2
	v_mov_b32_e32 v3, v2
	v_mov_b32_e32 v4, v2
	v_mov_b32_e32 v5, v2
	v_mov_b32_e32 v6, v2
	v_mov_b32_e32 v7, v2
	v_mov_b32_e32 v8, v2
	v_mov_b32_e32 v9, v2
	v_mov_b32_e32 v18, v2
	v_mov_b32_e32 v19, v2
	v_mov_b32_e32 v20, v2
	v_mov_b32_e32 v21, v2
	v_mov_b32_e32 v22, v2
	v_mov_b32_e32 v23, v2
	v_mov_b32_e32 v24, v2
	v_mov_b32_e32 v25, v2
	v_mov_b32_e32 v34, v2
	v_mov_b32_e32 v35, v2
	v_mov_b32_e32 v36, v2
	v_mov_b32_e32 v37, v2
	v_mov_b32_e32 v38, v2
	v_mov_b32_e32 v39, v2
	v_mov_b32_e32 v40, v2
	v_mov_b32_e32 v41, v2
	v_mov_b32_e32 v50, v2
	v_mov_b32_e32 v51, v2
	v_mov_b32_e32 v52, v2
	v_mov_b32_e32 v53, v2
	v_mov_b32_e32 v54, v2
	v_mov_b32_e32 v55, v2
	v_mov_b32_e32 v56, v2
	v_mov_b32_e32 v57, v2
	v_mov_b32_e32 v10, v2
	v_mov_b32_e32 v11, v2
	v_mov_b32_e32 v12, v2
	v_mov_b32_e32 v13, v2
	v_mov_b32_e32 v14, v2
	v_mov_b32_e32 v15, v2
	v_mov_b32_e32 v16, v2
	v_mov_b32_e32 v17, v2
	v_mov_b32_e32 v26, v2
	v_mov_b32_e32 v27, v2
	v_mov_b32_e32 v28, v2
	v_mov_b32_e32 v29, v2
	v_mov_b32_e32 v30, v2
	v_mov_b32_e32 v31, v2
	v_mov_b32_e32 v32, v2
	v_mov_b32_e32 v33, v2
	v_mov_b32_e32 v42, v2
	v_mov_b32_e32 v43, v2
	v_mov_b32_e32 v44, v2
	v_mov_b32_e32 v45, v2
	v_mov_b32_e32 v46, v2
	v_mov_b32_e32 v47, v2
	v_mov_b32_e32 v48, v2
	v_mov_b32_e32 v49, v2
	v_mov_b32_e32 v58, v2
	v_mov_b32_e32 v59, v2
	v_mov_b32_e32 v60, v2
	v_mov_b32_e32 v61, v2
	v_mov_b32_e32 v62, v2
	v_mov_b32_e32 v63, v2
	v_mov_b32_e32 v64, v2
	v_mov_b32_e32 v65, v2
	v_mov_b32_e32 v66, v2
	v_mov_b32_e32 v67, v2
	v_mov_b32_e32 v68, v2
	v_mov_b32_e32 v69, v2
	v_mov_b32_e32 v70, v2
	v_mov_b32_e32 v71, v2
	v_mov_b32_e32 v72, v2
	v_mov_b32_e32 v73, v2
	v_mov_b32_e32 v82, v2
	v_mov_b32_e32 v83, v2
	v_mov_b32_e32 v84, v2
	v_mov_b32_e32 v85, v2
	v_mov_b32_e32 v86, v2
	v_mov_b32_e32 v87, v2
	v_mov_b32_e32 v88, v2
	v_mov_b32_e32 v89, v2
	v_mov_b32_e32 v98, v2
	v_mov_b32_e32 v99, v2
	v_mov_b32_e32 v100, v2
	v_mov_b32_e32 v101, v2
	v_mov_b32_e32 v102, v2
	v_mov_b32_e32 v103, v2
	v_mov_b32_e32 v104, v2
	v_mov_b32_e32 v105, v2
	v_mov_b32_e32 v114, v2
	v_mov_b32_e32 v115, v2
	v_mov_b32_e32 v116, v2
	v_mov_b32_e32 v117, v2
	v_mov_b32_e32 v118, v2
	v_mov_b32_e32 v119, v2
	v_mov_b32_e32 v120, v2
	v_mov_b32_e32 v121, v2
	v_mov_b32_e32 v74, v2
	v_mov_b32_e32 v75, v2
	v_mov_b32_e32 v76, v2
	v_mov_b32_e32 v77, v2
	v_mov_b32_e32 v78, v2
	v_mov_b32_e32 v79, v2
	v_mov_b32_e32 v80, v2
	v_mov_b32_e32 v81, v2
	v_mov_b32_e32 v90, v2
	v_mov_b32_e32 v91, v2
	v_mov_b32_e32 v92, v2
	v_mov_b32_e32 v93, v2
	v_mov_b32_e32 v94, v2
	v_mov_b32_e32 v95, v2
	v_mov_b32_e32 v96, v2
	v_mov_b32_e32 v97, v2
	v_mov_b32_e32 v106, v2
	v_mov_b32_e32 v107, v2
	v_mov_b32_e32 v108, v2
	v_mov_b32_e32 v109, v2
	v_mov_b32_e32 v110, v2
	v_mov_b32_e32 v111, v2
	v_mov_b32_e32 v112, v2
	v_mov_b32_e32 v113, v2
	v_mov_b32_e32 v122, v2
	v_mov_b32_e32 v123, v2
	v_mov_b32_e32 v124, v2
	v_mov_b32_e32 v125, v2
	v_mov_b32_e32 v126, v2
	v_mov_b32_e32 v127, v2
	v_mov_b32_e32 v128, v2
	v_mov_b32_e32 v129, v2
	.p2align	6

.LBB0_214:
	s_ashr_i32 s23, s22, 31
	s_lshl_b64 s[4:5], s[22:23], 18
	s_add_u32 s24, s36, s4
	s_addc_u32 s25, s37, s5
	s_and_b64 s[4:5], s[8:9], exec
	s_cselect_b32 s23, s25, s29
	s_cselect_b32 s75, s24, s28
	s_ashr_i32 s21, s20, 31
	s_lshl_b64 s[4:5], s[20:21], 18
	s_add_u32 s26, s40, s4
	s_addc_u32 s27, s41, s5
	s_and_b64 s[4:5], s[8:9], exec
	s_cselect_b32 s21, s27, s31
	s_cselect_b32 s80, s26, s30
	s_add_u32 s28, s28, 0x20080
	s_addc_u32 s29, s29, 0
	s_add_u32 s88, s30, 0x100
	v_mov_b32_e32 v2, 0
	s_addc_u32 s89, s31, 0
	s_mov_b32 s96, -2
	v_mov_b32_e32 v3, v2
	v_mov_b32_e32 v4, v2
	v_mov_b32_e32 v5, v2
	v_mov_b32_e32 v6, v2
	v_mov_b32_e32 v7, v2
	v_mov_b32_e32 v8, v2
	v_mov_b32_e32 v9, v2
	v_mov_b32_e32 v10, v2
	v_mov_b32_e32 v11, v2
	v_mov_b32_e32 v12, v2
	v_mov_b32_e32 v13, v2
	v_mov_b32_e32 v14, v2
	v_mov_b32_e32 v15, v2
	v_mov_b32_e32 v16, v2
	v_mov_b32_e32 v17, v2
	v_mov_b32_e32 v18, v2
	v_mov_b32_e32 v19, v2
	v_mov_b32_e32 v20, v2
	v_mov_b32_e32 v21, v2
	v_mov_b32_e32 v22, v2
	v_mov_b32_e32 v23, v2
	v_mov_b32_e32 v24, v2
	v_mov_b32_e32 v25, v2
	v_mov_b32_e32 v26, v2
	v_mov_b32_e32 v27, v2
	v_mov_b32_e32 v28, v2
	v_mov_b32_e32 v29, v2
	v_mov_b32_e32 v30, v2
	v_mov_b32_e32 v31, v2
	v_mov_b32_e32 v32, v2
	v_mov_b32_e32 v33, v2
	v_mov_b32_e32 v66, v2
	v_mov_b32_e32 v67, v2
	v_mov_b32_e32 v68, v2
	v_mov_b32_e32 v69, v2
	v_mov_b32_e32 v70, v2
	v_mov_b32_e32 v71, v2
	v_mov_b32_e32 v72, v2
	v_mov_b32_e32 v73, v2
	v_mov_b32_e32 v74, v2
	v_mov_b32_e32 v75, v2
	v_mov_b32_e32 v76, v2
	v_mov_b32_e32 v77, v2
	v_mov_b32_e32 v78, v2
	v_mov_b32_e32 v79, v2
	v_mov_b32_e32 v80, v2
	v_mov_b32_e32 v81, v2
	v_mov_b32_e32 v82, v2
	v_mov_b32_e32 v83, v2
	v_mov_b32_e32 v84, v2
	v_mov_b32_e32 v85, v2
	v_mov_b32_e32 v86, v2
	v_mov_b32_e32 v87, v2
	v_mov_b32_e32 v88, v2
	v_mov_b32_e32 v89, v2
	v_mov_b32_e32 v90, v2
	v_mov_b32_e32 v91, v2
	v_mov_b32_e32 v92, v2
	v_mov_b32_e32 v93, v2
	v_mov_b32_e32 v94, v2
	v_mov_b32_e32 v95, v2
	v_mov_b32_e32 v96, v2
	v_mov_b32_e32 v97, v2
	v_mov_b32_e32 v34, v2
	v_mov_b32_e32 v35, v2
	v_mov_b32_e32 v36, v2
	v_mov_b32_e32 v37, v2
	v_mov_b32_e32 v38, v2
	v_mov_b32_e32 v39, v2
	v_mov_b32_e32 v40, v2
	v_mov_b32_e32 v41, v2
	v_mov_b32_e32 v42, v2
	v_mov_b32_e32 v43, v2
	v_mov_b32_e32 v44, v2
	v_mov_b32_e32 v45, v2
	v_mov_b32_e32 v46, v2
	v_mov_b32_e32 v47, v2
	v_mov_b32_e32 v48, v2
	v_mov_b32_e32 v49, v2
	v_mov_b32_e32 v50, v2
	v_mov_b32_e32 v51, v2
	v_mov_b32_e32 v52, v2
	v_mov_b32_e32 v53, v2
	v_mov_b32_e32 v54, v2
	v_mov_b32_e32 v55, v2
	v_mov_b32_e32 v56, v2
	v_mov_b32_e32 v57, v2
	v_mov_b32_e32 v58, v2
	v_mov_b32_e32 v59, v2
	v_mov_b32_e32 v60, v2
	v_mov_b32_e32 v61, v2
	v_mov_b32_e32 v62, v2
	v_mov_b32_e32 v63, v2
	v_mov_b32_e32 v64, v2
	v_mov_b32_e32 v65, v2
	v_mov_b32_e32 v98, v2
	v_mov_b32_e32 v99, v2
	v_mov_b32_e32 v100, v2
	v_mov_b32_e32 v101, v2
	v_mov_b32_e32 v102, v2
	v_mov_b32_e32 v103, v2
	v_mov_b32_e32 v104, v2
	v_mov_b32_e32 v105, v2
	v_mov_b32_e32 v106, v2
	v_mov_b32_e32 v107, v2
	v_mov_b32_e32 v108, v2
	v_mov_b32_e32 v109, v2
	v_mov_b32_e32 v110, v2
	v_mov_b32_e32 v111, v2
	v_mov_b32_e32 v112, v2
	v_mov_b32_e32 v113, v2
	v_mov_b32_e32 v114, v2
	v_mov_b32_e32 v115, v2
	v_mov_b32_e32 v116, v2
	v_mov_b32_e32 v117, v2
	v_mov_b32_e32 v118, v2
	v_mov_b32_e32 v119, v2
	v_mov_b32_e32 v120, v2
	v_mov_b32_e32 v121, v2
	v_mov_b32_e32 v122, v2
	v_mov_b32_e32 v123, v2
	v_mov_b32_e32 v124, v2
	v_mov_b32_e32 v125, v2
	v_mov_b32_e32 v126, v2
	v_mov_b32_e32 v127, v2
	v_mov_b32_e32 v128, v2
	v_mov_b32_e32 v129, v2
	.p2align	6

.LBB0_425:
	s_add_i32 s26, s26, 64
	v_cmp_eq_u32_e32 vcc, s26, v248
	v_add_u32_e32 v250, 0x100, v250
	v_lshl_add_u64 v[216:217], v[216:217], 0, s[86:87]
	v_lshl_add_u64 v[218:219], v[218:219], 0, s[56:57]
	s_add_i32 s25, s25, 1
	s_cbranch_vccnz .LBB0_450
	.p2align	6

.LBB0_545:
	s_or_b64 exec, exec, s[6:7]
	s_mov_b64 s[6:7], s[0:1]
	s_waitcnt lgkmcnt(0)
	s_barrier
	s_load_dwordx2 s[6:7], s[6:7], 0xd0
	v_mbcnt_lo_u32_b32 v0, -1, 0
	v_mbcnt_hi_u32_b32 v0, -1, v0
	s_movk_i32 s5, 0x13c0
	v_add_u32_e32 v0, s67, v0
	s_waitcnt lgkmcnt(0)
	s_add_u32 s26, s6, 0x11c00000
	s_addc_u32 s27, s7, 0
	s_ashr_i32 s35, s34, 31
	s_lshl_b64 s[36:37], s[34:35], 6
	s_sub_i32 s4, 14, s4
	v_lshlrev_b32_e32 v2, 3, v0
	v_add_u32_e32 v4, 0x200, v0
	s_add_u32 s28, s36, -15
	v_and_b32_e32 v14, 0x1f8, v2
	v_ashrrev_i32_e32 v2, 6, v0
	v_ashrrev_i32_e32 v4, 6, v4
	s_addc_u32 s29, s37, -1
	v_cmp_gt_i32_e32 vcc, s5, v0
	v_cmp_lt_i32_e64 s[6:7], s4, v2
	v_ashrrev_i32_e32 v3, 31, v2
	v_ashrrev_i32_e32 v5, 31, v4
	v_lshl_add_u64 v[2:3], s[28:29], 0, v[2:3]
	s_and_b64 s[24:25], vcc, s[6:7]
	s_movk_i32 s5, 0x11c0
	v_cmp_lt_i32_e64 s[6:7], s4, v4
	v_lshl_add_u64 v[4:5], s[28:29], 0, v[4:5]
	v_lshlrev_b64 v[2:3], 9, v[2:3]
	v_cmp_gt_i32_e32 vcc, s5, v0
	v_lshlrev_b64 v[4:5], 9, v[4:5]
	v_or_b32_e32 v2, v2, v14
	v_or_b32_e32 v4, v4, v14
	s_and_b64 s[22:23], vcc, s[6:7]
	v_cndmask_b32_e64 v3, 0, v3, s[24:25]
	v_cndmask_b32_e64 v2, 0, v2, s[24:25]
	v_cndmask_b32_e64 v5, 0, v5, s[22:23]
	v_cndmask_b32_e64 v4, 0, v4, s[22:23]
	v_lshl_add_u64 v[2:3], v[2:3], 1, s[26:27]
	v_lshl_add_u64 v[4:5], v[4:5], 1, s[26:27]
	global_load_dwordx4 v[38:41], v[2:3], off
	global_load_dwordx4 v[26:29], v[4:5], off
	v_add_u32_e32 v2, 0x400, v0
	v_add_u32_e32 v4, 0x600, v0
	v_ashrrev_i32_e32 v2, 6, v2
	s_movk_i32 s5, 0xfc0
	v_ashrrev_i32_e32 v4, 6, v4
	v_cmp_gt_i32_e32 vcc, s5, v0
	v_cmp_lt_i32_e64 s[6:7], s4, v2
	v_ashrrev_i32_e32 v3, 31, v2
	v_ashrrev_i32_e32 v5, 31, v4
	v_lshl_add_u64 v[2:3], s[28:29], 0, v[2:3]
	s_and_b64 s[20:21], vcc, s[6:7]
	s_movk_i32 s5, 0xdc0
	v_cmp_lt_i32_e64 s[6:7], s4, v4
	v_lshl_add_u64 v[4:5], s[28:29], 0, v[4:5]
	v_lshlrev_b64 v[2:3], 9, v[2:3]
	v_cmp_gt_i32_e32 vcc, s5, v0
	v_lshlrev_b64 v[4:5], 9, v[4:5]
	v_or_b32_e32 v2, v2, v14
	v_or_b32_e32 v4, v4, v14
	s_and_b64 s[18:19], vcc, s[6:7]
	v_cndmask_b32_e64 v3, 0, v3, s[20:21]
	v_cndmask_b32_e64 v2, 0, v2, s[20:21]
	v_cndmask_b32_e64 v5, 0, v5, s[18:19]
	v_cndmask_b32_e64 v4, 0, v4, s[18:19]
	v_lshl_add_u64 v[2:3], v[2:3], 1, s[26:27]
	v_lshl_add_u64 v[4:5], v[4:5], 1, s[26:27]
	global_load_dwordx4 v[34:37], v[2:3], off
	global_load_dwordx4 v[18:21], v[4:5], off
	v_add_u32_e32 v2, 0x800, v0
	v_add_u32_e32 v4, 0xa00, v0
	v_ashrrev_i32_e32 v2, 6, v2
	s_movk_i32 s5, 0xbc0
	v_ashrrev_i32_e32 v4, 6, v4
	v_cmp_gt_i32_e32 vcc, s5, v0
	v_cmp_lt_i32_e64 s[6:7], s4, v2
	v_ashrrev_i32_e32 v3, 31, v2
	v_ashrrev_i32_e32 v5, 31, v4
	v_lshl_add_u64 v[2:3], s[28:29], 0, v[2:3]
	s_and_b64 s[16:17], vcc, s[6:7]
	s_movk_i32 s5, 0x9c0
	v_cmp_lt_i32_e64 s[6:7], s4, v4
	v_lshl_add_u64 v[4:5], s[28:29], 0, v[4:5]
	v_lshlrev_b64 v[2:3], 9, v[2:3]
	v_cmp_gt_i32_e32 vcc, s5, v0
	v_lshlrev_b64 v[4:5], 9, v[4:5]
	v_or_b32_e32 v2, v2, v14
	v_or_b32_e32 v4, v4, v14
	s_and_b64 s[14:15], vcc, s[6:7]
	v_cndmask_b32_e64 v3, 0, v3, s[16:17]
	v_cndmask_b32_e64 v2, 0, v2, s[16:17]
	v_cndmask_b32_e64 v5, 0, v5, s[14:15]
	v_cndmask_b32_e64 v4, 0, v4, s[14:15]
	v_lshl_add_u64 v[2:3], v[2:3], 1, s[26:27]
	v_lshl_add_u64 v[4:5], v[4:5], 1, s[26:27]
	global_load_dwordx4 v[30:33], v[2:3], off
	global_load_dwordx4 v[10:13], v[4:5], off
	v_add_u32_e32 v2, 0xc00, v0
	v_add_u32_e32 v4, 0xe00, v0
	v_ashrrev_i32_e32 v2, 6, v2
	s_movk_i32 s5, 0x7c0
	v_ashrrev_i32_e32 v4, 6, v4
	v_cmp_gt_i32_e32 vcc, s5, v0
	v_cmp_lt_i32_e64 s[6:7], s4, v2
	v_ashrrev_i32_e32 v3, 31, v2
	v_ashrrev_i32_e32 v5, 31, v4
	v_lshl_add_u64 v[2:3], s[28:29], 0, v[2:3]
	s_and_b64 s[12:13], vcc, s[6:7]
	s_movk_i32 s5, 0x5c0
	v_cmp_lt_i32_e64 s[6:7], s4, v4
	v_lshl_add_u64 v[4:5], s[28:29], 0, v[4:5]
	v_lshlrev_b64 v[2:3], 9, v[2:3]
	v_cmp_gt_i32_e32 vcc, s5, v0
	v_lshlrev_b64 v[4:5], 9, v[4:5]
	v_or_b32_e32 v2, v2, v14
	v_or_b32_e32 v4, v4, v14
	s_and_b64 s[10:11], vcc, s[6:7]
	v_cndmask_b32_e64 v3, 0, v3, s[12:13]
	v_cndmask_b32_e64 v2, 0, v2, s[12:13]
	v_cndmask_b32_e64 v5, 0, v5, s[10:11]
	v_cndmask_b32_e64 v4, 0, v4, s[10:11]
	v_lshl_add_u64 v[2:3], v[2:3], 1, s[26:27]
	v_lshl_add_u64 v[4:5], v[4:5], 1, s[26:27]
	global_load_dwordx4 v[22:25], v[2:3], off
	global_load_dwordx4 v[6:9], v[4:5], off
	v_add_u32_e32 v2, 0x1000, v0
	v_add_u32_e32 v4, 0x1200, v0
	v_ashrrev_i32_e32 v2, 6, v2
	s_movk_i32 s5, 0x3c0
	v_ashrrev_i32_e32 v4, 6, v4
	v_cmp_gt_i32_e32 vcc, s5, v0
	v_cmp_lt_i32_e64 s[6:7], s4, v2
	v_ashrrev_i32_e32 v3, 31, v2
	v_ashrrev_i32_e32 v5, 31, v4
	v_lshl_add_u64 v[2:3], s[28:29], 0, v[2:3]
	s_and_b64 s[8:9], vcc, s[6:7]
	s_movk_i32 s5, 0x1c0
	v_cmp_lt_i32_e64 s[6:7], s4, v4
	v_lshl_add_u64 v[4:5], s[28:29], 0, v[4:5]
	v_lshlrev_b64 v[2:3], 9, v[2:3]
	v_cmp_gt_i32_e32 vcc, s5, v0
	v_lshlrev_b64 v[4:5], 9, v[4:5]
	v_or_b32_e32 v2, v2, v14
	v_or_b32_e32 v0, v4, v14
	s_and_b64 s[6:7], vcc, s[6:7]
	v_cndmask_b32_e64 v3, 0, v3, s[8:9]
	v_cndmask_b32_e64 v2, 0, v2, s[8:9]
	v_cndmask_b32_e64 v5, 0, v5, s[6:7]
	v_cndmask_b32_e64 v4, 0, v0, s[6:7]
	v_lshl_add_u64 v[2:3], v[2:3], 1, s[26:27]
	v_lshl_add_u64 v[4:5], v[4:5], 1, s[26:27]
	global_load_dwordx4 v[14:17], v[2:3], off
	s_nop 0
	global_load_dwordx4 v[2:5], v[4:5], off
	s_mov_b64 s[4:5], s[0:1]
	s_load_dwordx2 s[28:29], s[4:5], 0xd0
	s_load_dwordx2 s[26:27], s[4:5], 0x58
	v_mbcnt_lo_u32_b32 v0, -1, 0
	v_mbcnt_hi_u32_b32 v0, -1, v0
	s_mov_b32 s30, 0
	v_add_u32_e32 v0, s67, v0
	s_mov_b32 s31, 1
	s_waitcnt vmcnt(10)
	v_mov_b32_e32 v43, v42
	v_lshl_add_u32 v222, v0, 1, 0
	v_mov_b32_e32 v153, v152
	v_mov_b32_e32 v45, v44
	v_mov_b32_e32 v47, v46
	v_mov_b32_e32 v49, v48
	v_mov_b32_e32 v51, v50
	v_mov_b32_e32 v53, v52
	v_mov_b32_e32 v55, v54
	v_mov_b32_e32 v57, v56
	v_mov_b32_e32 v59, v58
	v_mov_b32_e32 v61, v60
	v_mov_b32_e32 v63, v62
	v_mov_b32_e32 v65, v64
	v_mov_b32_e32 v115, v114
	v_mov_b32_e32 v117, v116
	v_mov_b32_e32 v119, v118
	v_mov_b32_e32 v121, v120
	v_mov_b32_e32 v123, v122
	v_mov_b32_e32 v125, v124
	v_mov_b32_e32 v127, v126
	v_mov_b32_e32 v129, v128
	v_mov_b32_e32 v131, v130
	v_mov_b32_e32 v133, v132
	v_mov_b32_e32 v135, v134
	v_mov_b32_e32 v137, v136
	v_mov_b32_e32 v139, v138
	v_mov_b32_e32 v141, v140
	v_mov_b32_e32 v143, v142
	v_mov_b32_e32 v145, v144
	v_mov_b32_e32 v147, v146
	v_mov_b32_e32 v149, v148
	v_mov_b32_e32 v151, v150
	s_mov_b32 s33, 8
	.p2align	6

.LBB0_882:
	s_ashr_i32 s23, s22, 31
	s_lshl_b64 s[4:5], s[22:23], 19
	s_add_u32 s24, s34, s4
	s_addc_u32 s25, s35, s5
	s_and_b64 s[4:5], s[8:9], exec
	s_cselect_b32 s23, s25, s11
	s_cselect_b32 s68, s24, s10
	s_ashr_i32 s21, s20, 31
	s_lshl_b64 s[4:5], s[20:21], 19
	s_add_u32 s26, s36, s4
	s_addc_u32 s27, s37, s5
	s_and_b64 s[4:5], s[8:9], exec
	s_cselect_b32 s21, s27, s29
	s_cselect_b32 s69, s26, s28
	s_add_u32 s10, s10, 0x40080
	s_addc_u32 s11, s11, 0
	s_add_u32 s70, s28, 0x100
	v_mov_b32_e32 v2, 0
	s_addc_u32 s71, s29, 0
	s_mov_b32 s75, -2
	v_mov_b32_e32 v3, v2
	v_mov_b32_e32 v4, v2
	v_mov_b32_e32 v5, v2
	v_mov_b32_e32 v6, v2
	v_mov_b32_e32 v7, v2
	v_mov_b32_e32 v8, v2
	v_mov_b32_e32 v9, v2
	v_mov_b32_e32 v10, v2
	v_mov_b32_e32 v11, v2
	v_mov_b32_e32 v12, v2
	v_mov_b32_e32 v13, v2
	v_mov_b32_e32 v18, v2
	v_mov_b32_e32 v19, v2
	v_mov_b32_e32 v20, v2
	v_mov_b32_e32 v21, v2
	v_mov_b32_e32 v26, v2
	v_mov_b32_e32 v27, v2
	v_mov_b32_e32 v28, v2
	v_mov_b32_e32 v29, v2
	v_mov_b32_e32 v34, v2
	v_mov_b32_e32 v35, v2
	v_mov_b32_e32 v36, v2
	v_mov_b32_e32 v37, v2
	v_mov_b32_e32 v42, v2
	v_mov_b32_e32 v43, v2
	v_mov_b32_e32 v44, v2
	v_mov_b32_e32 v45, v2
	v_mov_b32_e32 v50, v2
	v_mov_b32_e32 v51, v2
	v_mov_b32_e32 v52, v2
	v_mov_b32_e32 v53, v2
	v_mov_b32_e32 v14, v2
	v_mov_b32_e32 v15, v2
	v_mov_b32_e32 v16, v2
	v_mov_b32_e32 v17, v2
	v_mov_b32_e32 v22, v2
	v_mov_b32_e32 v23, v2
	v_mov_b32_e32 v24, v2
	v_mov_b32_e32 v25, v2
	v_mov_b32_e32 v30, v2
	v_mov_b32_e32 v31, v2
	v_mov_b32_e32 v32, v2
	v_mov_b32_e32 v33, v2
	v_mov_b32_e32 v38, v2
	v_mov_b32_e32 v39, v2
	v_mov_b32_e32 v40, v2
	v_mov_b32_e32 v41, v2
	v_mov_b32_e32 v46, v2
	v_mov_b32_e32 v47, v2
	v_mov_b32_e32 v48, v2
	v_mov_b32_e32 v49, v2
	v_mov_b32_e32 v54, v2
	v_mov_b32_e32 v55, v2
	v_mov_b32_e32 v56, v2
	v_mov_b32_e32 v57, v2
	v_mov_b32_e32 v58, v2
	v_mov_b32_e32 v59, v2
	v_mov_b32_e32 v60, v2
	v_mov_b32_e32 v61, v2
	v_mov_b32_e32 v62, v2
	v_mov_b32_e32 v63, v2
	v_mov_b32_e32 v64, v2
	v_mov_b32_e32 v65, v2
	s_waitcnt vmcnt(0)
	v_mov_b32_e32 v66, v2
	v_mov_b32_e32 v67, v2
	v_mov_b32_e32 v68, v2
	v_mov_b32_e32 v69, v2
	v_mov_b32_e32 v70, v2
	v_mov_b32_e32 v71, v2
	v_mov_b32_e32 v72, v2
	v_mov_b32_e32 v73, v2
	v_mov_b32_e32 v74, v2
	v_mov_b32_e32 v75, v2
	v_mov_b32_e32 v76, v2
	v_mov_b32_e32 v77, v2
	v_mov_b32_e32 v82, v2
	v_mov_b32_e32 v83, v2
	v_mov_b32_e32 v84, v2
	v_mov_b32_e32 v85, v2
	v_mov_b32_e32 v90, v2
	v_mov_b32_e32 v91, v2
	v_mov_b32_e32 v92, v2
	v_mov_b32_e32 v93, v2
	v_mov_b32_e32 v98, v2
	v_mov_b32_e32 v99, v2
	v_mov_b32_e32 v100, v2
	v_mov_b32_e32 v101, v2
	v_mov_b32_e32 v106, v2
	v_mov_b32_e32 v107, v2
	v_mov_b32_e32 v108, v2
	v_mov_b32_e32 v109, v2
	v_mov_b32_e32 v114, v2
	v_mov_b32_e32 v115, v2
	v_mov_b32_e32 v116, v2
	v_mov_b32_e32 v117, v2
	v_mov_b32_e32 v78, v2
	v_mov_b32_e32 v79, v2
	v_mov_b32_e32 v80, v2
	v_mov_b32_e32 v81, v2
	v_mov_b32_e32 v86, v2
	v_mov_b32_e32 v87, v2
	v_mov_b32_e32 v88, v2
	v_mov_b32_e32 v89, v2
	v_mov_b32_e32 v94, v2
	v_mov_b32_e32 v95, v2
	v_mov_b32_e32 v96, v2
	v_mov_b32_e32 v97, v2
	v_mov_b32_e32 v102, v2
	v_mov_b32_e32 v103, v2
	v_mov_b32_e32 v104, v2
	v_mov_b32_e32 v105, v2
	v_mov_b32_e32 v110, v2
	v_mov_b32_e32 v111, v2
	v_mov_b32_e32 v112, v2
	v_mov_b32_e32 v113, v2
	v_mov_b32_e32 v118, v2
	v_mov_b32_e32 v119, v2
	v_mov_b32_e32 v120, v2
	v_mov_b32_e32 v121, v2
	v_mov_b32_e32 v122, v2
	v_mov_b32_e32 v123, v2
	v_mov_b32_e32 v124, v2
	v_mov_b32_e32 v125, v2
	v_mov_b32_e32 v126, v2
	v_mov_b32_e32 v127, v2
	v_mov_b32_e32 v128, v2
	v_mov_b32_e32 v129, v2
	.p2align	6

.LBB0_1173:
	s_ashr_i32 s17, s16, 31
	s_lshl_b64 s[22:23], s[16:17], 18
	s_add_u32 s22, s62, s22
	s_addc_u32 s23, s63, s23
	s_and_b64 s[24:25], s[18:19], exec
	s_cselect_b32 s17, s23, s35
	s_cselect_b32 vcc_lo, s22, s34
	s_ashr_i32 s21, s20, 31
	s_lshl_b64 s[24:25], s[20:21], 18
	s_add_u32 s24, s70, s24
	s_addc_u32 s25, s71, s25
	s_and_b64 s[36:37], s[18:19], exec
	s_cselect_b32 s21, s25, s31
	s_cselect_b32 vcc_hi, s24, s30
	s_add_i32 s50, 0, 0x10000
	s_add_i32 s94, 0, 0x14000
	v_add_u32_e32 v140, s50, v144
	v_add_u32_e32 v141, s94, v144
	ds_read_b128 v[2:5], v140
	ds_read_b128 v[6:9], v140 offset:1024
	ds_read_b128 v[10:13], v140 offset:2048
	ds_read_b128 v[14:17], v140 offset:3072
	ds_read_b128 v[18:21], v141
	ds_read_b128 v[22:25], v141 offset:1024
	ds_read_b128 v[26:29], v141 offset:2048
	ds_read_b128 v[30:33], v141 offset:3072
	s_mov_b32 s68, s65
	s_mov_b32 s65, s77
	s_mov_b32 s55, s76
	s_add_u32 s36, s34, 0x20080
	s_addc_u32 s37, s35, 0
	s_add_i32 s27, s4, 0xc000
	v_lshl_add_u64 v[66:67], s[36:37], 0, v[130:131]
	s_mov_b32 m0, s27
	s_add_i32 s90, s4, 0xe000
	ds_read_b128 v[34:37], v145
	ds_read_b128 v[38:41], v145 offset:1024
	ds_read_b128 v[42:45], v145 offset:2048
	ds_read_b128 v[46:49], v145 offset:3072
	ds_read_b128 v[50:53], v145 offset:4096
	ds_read_b128 v[54:57], v145 offset:5120
	ds_read_b128 v[58:61], v145 offset:6144
	ds_read_b128 v[62:65], v145 offset:7168
	global_load_lds_dwordx4 v[66:67], off
	v_lshl_add_u64 v[66:67], s[36:37], 0, v[132:133]
	s_mov_b32 m0, s90
	s_nop 0
	global_load_lds_dwordx4 v[66:67], off
	s_waitcnt vmcnt(8)
	s_waitcnt lgkmcnt(0)
	s_barrier
	s_setprio 1
	s_waitcnt lgkmcnt(0)
	v_mfma_i32_16x16x64_i8 v[90:93], v[2:5], v[58:61], 0
	s_mov_b32 s5, 0
	v_mfma_i32_16x16x64_i8 v[66:69], v[2:5], v[34:37], 0
	v_mfma_i32_16x16x64_i8 v[70:73], v[10:13], v[34:37], 0
	v_mfma_i32_16x16x64_i8 v[74:77], v[2:5], v[42:45], 0
	v_mfma_i32_16x16x64_i8 v[78:81], v[10:13], v[42:45], 0
	v_mfma_i32_16x16x64_i8 v[82:85], v[2:5], v[50:53], 0
	v_mfma_i32_16x16x64_i8 v[86:89], v[10:13], v[50:53], 0
	v_mfma_i32_16x16x64_i8 v[94:97], v[6:9], v[62:65], v[90:93]
	v_mfma_i32_16x16x64_i8 v[90:93], v[10:13], v[58:61], 0
	v_mfma_i32_16x16x64_i8 v[66:69], v[6:9], v[38:41], v[66:69]
	v_mfma_i32_16x16x64_i8 v[70:73], v[14:17], v[38:41], v[70:73]
	v_mfma_i32_16x16x64_i8 v[74:77], v[6:9], v[46:49], v[74:77]
	v_mfma_i32_16x16x64_i8 v[78:81], v[14:17], v[46:49], v[78:81]
	v_mfma_i32_16x16x64_i8 v[82:85], v[6:9], v[54:57], v[82:85]
	v_mfma_i32_16x16x64_i8 v[86:89], v[14:17], v[54:57], v[86:89]
	v_mfma_i32_16x16x64_i8 v[98:101], v[14:17], v[62:65], v[90:93]
	s_setprio 0
	s_setprio 1
	v_mfma_i32_16x16x64_i8 v[90:93], v[18:21], v[34:37], 0
	v_mfma_i32_16x16x64_i8 v[34:37], v[26:29], v[34:37], 0
	v_mfma_i32_16x16x64_i8 v[110:113], v[22:25], v[38:41], v[90:93]
	v_mfma_i32_16x16x64_i8 v[34:37], v[30:33], v[38:41], v[34:37]
	v_mfma_i32_16x16x64_i8 v[38:41], v[18:21], v[42:45], 0
	v_mfma_i32_16x16x64_i8 v[42:45], v[26:29], v[42:45], 0
	v_mfma_i32_16x16x64_i8 v[38:41], v[22:25], v[46:49], v[38:41]
	v_mfma_i32_16x16x64_i8 v[42:45], v[30:33], v[46:49], v[42:45]
	v_mfma_i32_16x16x64_i8 v[46:49], v[18:21], v[50:53], 0
	v_mfma_i32_16x16x64_i8 v[50:53], v[26:29], v[50:53], 0
	v_mfma_i32_16x16x64_i8 v[46:49], v[22:25], v[54:57], v[46:49]
	v_mfma_i32_16x16x64_i8 v[50:53], v[30:33], v[54:57], v[50:53]
	v_mfma_i32_16x16x64_i8 v[54:57], v[18:21], v[58:61], 0
	v_mfma_i32_16x16x64_i8 v[58:61], v[26:29], v[58:61], 0
	v_mfma_i32_16x16x64_i8 v[54:57], v[22:25], v[62:65], v[54:57]
	v_mfma_i32_16x16x64_i8 v[58:61], v[30:33], v[62:65], v[58:61]
	s_setprio 0
	s_barrier
	s_add_i32 s50, s50, s75
	v_lshl_add_u64 v[230:231], s[30:31], 0, v[0:1]
	s_add_i32 s51, s50, 0x2000
	v_lshl_add_u64 v[142:143], v[230:231], 0, s[92:93]
	s_mov_b32 m0, s50
	v_lshl_add_u64 v[232:233], s[30:31], 0, v[134:135]
	s_add_u32 s36, s30, 0x20100
	ds_read_b128 v[62:65], v145 offset:16384
	ds_read_b128 v[90:93], v145 offset:17408
	ds_read_b128 v[102:105], v145 offset:18432
	ds_read_b128 v[106:109], v145 offset:19456
	ds_read_b128 v[114:117], v145 offset:20480
	ds_read_b128 v[118:121], v145 offset:21504
	ds_read_b128 v[122:125], v145 offset:22528
	ds_read_b128 v[126:129], v145 offset:23552
	global_load_lds_dwordx4 v[142:143], off
	v_lshl_add_u64 v[142:143], v[232:233], 0, s[92:93]
	s_mov_b32 m0, s51
	s_addc_u32 s37, s31, 0
	s_add_i32 s94, s94, s75
	global_load_lds_dwordx4 v[142:143], off
	v_lshl_add_u64 v[142:143], s[36:37], 0, v[0:1]
	s_mov_b32 m0, s94
	s_add_i32 s95, s94, 0x2000
	global_load_lds_dwordx4 v[142:143], off
	v_lshl_add_u64 v[142:143], s[36:37], 0, v[134:135]
	s_mov_b32 m0, s95
	v_lshl_add_u64 v[244:245], s[34:35], 0, v[130:131]
	global_load_lds_dwordx4 v[142:143], off
	v_lshl_add_u64 v[142:143], v[244:245], 0, s[92:93]
	s_mov_b32 m0, s4
	v_lshl_add_u64 v[246:247], s[34:35], 0, v[132:133]
	global_load_lds_dwordx4 v[142:143], off
	v_lshl_add_u64 v[142:143], v[246:247], 0, s[92:93]
	s_mov_b32 m0, s29
	s_nop 0
	global_load_lds_dwordx4 v[142:143], off
	s_waitcnt vmcnt(8)
	s_waitcnt lgkmcnt(0)
	s_barrier
	s_setprio 1
	s_waitcnt lgkmcnt(0)
	v_mfma_i32_16x16x64_i8 v[146:149], v[2:5], v[62:65], 0
	v_mfma_i32_16x16x64_i8 v[154:157], v[2:5], v[102:105], 0
	v_mfma_i32_16x16x64_i8 v[162:165], v[2:5], v[114:117], 0
	v_mfma_i32_16x16x64_i8 v[2:5], v[2:5], v[122:125], 0
	v_mfma_i32_16x16x64_i8 v[146:149], v[6:9], v[90:93], v[146:149]
	v_mfma_i32_16x16x64_i8 v[154:157], v[6:9], v[106:109], v[154:157]
	v_mfma_i32_16x16x64_i8 v[162:165], v[6:9], v[118:121], v[162:165]
	v_mfma_i32_16x16x64_i8 v[2:5], v[6:9], v[126:129], v[2:5]
	v_mfma_i32_16x16x64_i8 v[6:9], v[10:13], v[122:125], 0
	v_mfma_i32_16x16x64_i8 v[150:153], v[10:13], v[62:65], 0
	v_mfma_i32_16x16x64_i8 v[158:161], v[10:13], v[102:105], 0
	v_mfma_i32_16x16x64_i8 v[166:169], v[10:13], v[114:117], 0
	v_mfma_i32_16x16x64_i8 v[6:9], v[14:17], v[126:129], v[6:9]
	v_mfma_i32_16x16x64_i8 v[150:153], v[14:17], v[90:93], v[150:153]
	v_mfma_i32_16x16x64_i8 v[158:161], v[14:17], v[106:109], v[158:161]
	v_mfma_i32_16x16x64_i8 v[166:169], v[14:17], v[118:121], v[166:169]
	s_setprio 0
	s_setprio 1
	v_mfma_i32_16x16x64_i8 v[10:13], v[18:21], v[62:65], 0
	v_mfma_i32_16x16x64_i8 v[14:17], v[22:25], v[90:93], v[10:13]
	v_mfma_i32_16x16x64_i8 v[10:13], v[26:29], v[62:65], 0
	v_mfma_i32_16x16x64_i8 v[170:173], v[30:33], v[90:93], v[10:13]
	v_mfma_i32_16x16x64_i8 v[10:13], v[18:21], v[102:105], 0
	v_mfma_i32_16x16x64_i8 v[174:177], v[22:25], v[106:109], v[10:13]
	v_mfma_i32_16x16x64_i8 v[10:13], v[26:29], v[102:105], 0
	v_mfma_i32_16x16x64_i8 v[178:181], v[30:33], v[106:109], v[10:13]
	v_mfma_i32_16x16x64_i8 v[10:13], v[18:21], v[114:117], 0
	v_mfma_i32_16x16x64_i8 v[182:185], v[22:25], v[118:121], v[10:13]
	v_mfma_i32_16x16x64_i8 v[10:13], v[26:29], v[114:117], 0
	v_mfma_i32_16x16x64_i8 v[186:189], v[30:33], v[118:121], v[10:13]
	v_mfma_i32_16x16x64_i8 v[10:13], v[18:21], v[122:125], 0
	v_mfma_i32_16x16x64_i8 v[190:193], v[22:25], v[126:129], v[10:13]
	v_mfma_i32_16x16x64_i8 v[10:13], v[26:29], v[122:125], 0
	v_mfma_i32_16x16x64_i8 v[194:197], v[30:33], v[126:129], v[10:13]
	s_setprio 0
	s_barrier
	s_add_i32 s78, 0, 0x18000
	s_add_i32 s58, 0, 0x1c000
	v_add_u32_e32 v142, s78, v144
	v_add_u32_e32 v143, s58, v144
	s_nop 0
	ds_read_b128 v[10:13], v142
	ds_read_b128 v[18:21], v142 offset:1024
	ds_read_b128 v[30:33], v142 offset:2048
	ds_read_b128 v[62:65], v142 offset:3072
	ds_read_b128 v[198:201], v143
	ds_read_b128 v[202:205], v143 offset:1024
	ds_read_b128 v[206:209], v143 offset:2048
	ds_read_b128 v[210:213], v143 offset:3072
	s_add_u32 s36, s34, 0x20100
	s_addc_u32 s37, s35, 0
	s_mov_b32 m0, s96
	v_lshl_add_u64 v[90:91], s[36:37], 0, v[130:131]
	ds_read_b128 v[22:25], v145 offset:32768
	ds_read_b128 v[26:29], v145 offset:33792
	ds_read_b128 v[214:217], v145 offset:34816
	ds_read_b128 v[218:221], v145 offset:35840
	ds_read_b128 v[222:225], v145 offset:36864
	ds_read_b128 v[226:229], v145 offset:37888
	ds_read_b128 v[240:243], v145 offset:38912
	ds_read_b128 v[248:251], v145 offset:39936
	global_load_lds_dwordx4 v[90:91], off
	v_lshl_add_u64 v[90:91], s[36:37], 0, v[132:133]
	s_mov_b32 m0, s44
	s_nop 0
	global_load_lds_dwordx4 v[90:91], off
	s_waitcnt vmcnt(8)
	s_waitcnt lgkmcnt(0)
	s_barrier
	s_setprio 1
	s_waitcnt lgkmcnt(0)
	v_mfma_i32_16x16x64_i8 v[66:69], v[10:13], v[22:25], v[66:69]
	v_mfma_i32_16x16x64_i8 v[122:125], v[18:21], v[26:29], v[66:69]
	v_mfma_i32_16x16x64_i8 v[66:69], v[30:33], v[22:25], v[70:73]
	v_mfma_i32_16x16x64_i8 v[118:121], v[62:65], v[26:29], v[66:69]
	v_mfma_i32_16x16x64_i8 v[66:69], v[10:13], v[214:217], v[74:77]
	v_mfma_i32_16x16x64_i8 v[106:109], v[18:21], v[218:221], v[66:69]
	v_mfma_i32_16x16x64_i8 v[66:69], v[30:33], v[214:217], v[78:81]
	v_mfma_i32_16x16x64_i8 v[102:105], v[62:65], v[218:221], v[66:69]
	v_mfma_i32_16x16x64_i8 v[66:69], v[10:13], v[222:225], v[82:85]
	v_mfma_i32_16x16x64_i8 v[90:93], v[18:21], v[226:229], v[66:69]
	v_mfma_i32_16x16x64_i8 v[66:69], v[30:33], v[222:225], v[86:89]
	v_mfma_i32_16x16x64_i8 v[86:89], v[62:65], v[226:229], v[66:69]
	v_mfma_i32_16x16x64_i8 v[66:69], v[10:13], v[240:243], v[94:97]
	v_mfma_i32_16x16x64_i8 v[74:77], v[18:21], v[248:251], v[66:69]
	v_mfma_i32_16x16x64_i8 v[66:69], v[30:33], v[240:243], v[98:101]
	v_mfma_i32_16x16x64_i8 v[70:73], v[62:65], v[248:251], v[66:69]
	s_setprio 0
	s_setprio 1
	v_mfma_i32_16x16x64_i8 v[66:69], v[198:201], v[22:25], v[110:113]
	v_mfma_i32_16x16x64_i8 v[22:25], v[206:209], v[22:25], v[34:37]
	v_mfma_i32_16x16x64_i8 v[114:117], v[210:213], v[26:29], v[22:25]
	v_mfma_i32_16x16x64_i8 v[22:25], v[198:201], v[214:217], v[38:41]
	v_mfma_i32_16x16x64_i8 v[110:113], v[202:205], v[218:221], v[22:25]
	v_mfma_i32_16x16x64_i8 v[22:25], v[206:209], v[214:217], v[42:45]
	v_mfma_i32_16x16x64_i8 v[98:101], v[210:213], v[218:221], v[22:25]
	v_mfma_i32_16x16x64_i8 v[22:25], v[198:201], v[222:225], v[46:49]
	v_mfma_i32_16x16x64_i8 v[94:97], v[202:205], v[226:229], v[22:25]
	v_mfma_i32_16x16x64_i8 v[22:25], v[206:209], v[222:225], v[50:53]
	v_mfma_i32_16x16x64_i8 v[82:85], v[210:213], v[226:229], v[22:25]
	v_mfma_i32_16x16x64_i8 v[22:25], v[198:201], v[240:243], v[54:57]
	v_mfma_i32_16x16x64_i8 v[78:81], v[202:205], v[248:251], v[22:25]
	v_mfma_i32_16x16x64_i8 v[22:25], v[206:209], v[240:243], v[58:61]
	v_mfma_i32_16x16x64_i8 v[126:129], v[202:205], v[26:29], v[66:69]
	v_mfma_i32_16x16x64_i8 v[66:69], v[210:213], v[248:251], v[22:25]
	s_setprio 0
	s_barrier
	s_add_i32 s78, s78, s75
	s_mov_b64 s[76:77], 0x180
	s_add_i32 s79, s78, 0x2000
	s_nop 0
	v_lshl_add_u64 v[22:23], v[230:231], 0, s[76:77]
	s_mov_b32 m0, s78
	s_add_u32 s36, s30, 0x20180
	ds_read_b128 v[34:37], v145 offset:49152
	ds_read_b128 v[46:49], v145 offset:50176
	ds_read_b128 v[214:217], v145 offset:51200
	ds_read_b128 v[218:221], v145 offset:52224
	ds_read_b128 v[222:225], v145 offset:53248
	ds_read_b128 v[226:229], v145 offset:54272
	ds_read_b128 v[240:243], v145 offset:55296
	ds_read_b128 v[248:251], v145 offset:56320
	global_load_lds_dwordx4 v[22:23], off
	v_lshl_add_u64 v[22:23], v[232:233], 0, s[76:77]
	s_mov_b32 m0, s79
	s_addc_u32 s37, s31, 0
	s_add_i32 s58, s58, s75
	global_load_lds_dwordx4 v[22:23], off
	v_lshl_add_u64 v[22:23], s[36:37], 0, v[0:1]
	s_mov_b32 m0, s58
	s_add_i32 s48, s58, 0x2000
	global_load_lds_dwordx4 v[22:23], off
	v_lshl_add_u64 v[22:23], s[36:37], 0, v[134:135]
	s_mov_b32 m0, s48
	s_nop 0
	global_load_lds_dwordx4 v[22:23], off
	v_lshl_add_u64 v[22:23], v[244:245], 0, s[76:77]
	s_mov_b32 m0, s88
	s_nop 0
	global_load_lds_dwordx4 v[22:23], off
	v_lshl_add_u64 v[22:23], v[246:247], 0, s[76:77]
	s_mov_b32 m0, s89
	s_nop 0
	global_load_lds_dwordx4 v[22:23], off
	s_waitcnt vmcnt(8)
	s_waitcnt lgkmcnt(0)
	s_barrier
	s_setprio 1
	s_waitcnt lgkmcnt(0)
	v_mfma_i32_16x16x64_i8 v[22:25], v[10:13], v[34:37], v[146:149]
	v_mfma_i32_16x16x64_i8 v[58:61], v[18:21], v[46:49], v[22:25]
	v_mfma_i32_16x16x64_i8 v[22:25], v[30:33], v[34:37], v[150:153]
	v_mfma_i32_16x16x64_i8 v[54:57], v[62:65], v[46:49], v[22:25]
	v_mfma_i32_16x16x64_i8 v[22:25], v[10:13], v[214:217], v[154:157]
	v_mfma_i32_16x16x64_i8 v[42:45], v[18:21], v[218:221], v[22:25]
	v_mfma_i32_16x16x64_i8 v[22:25], v[30:33], v[214:217], v[158:161]
	v_mfma_i32_16x16x64_i8 v[38:41], v[62:65], v[218:221], v[22:25]
	v_mfma_i32_16x16x64_i8 v[22:25], v[10:13], v[222:225], v[162:165]
	v_mfma_i32_16x16x64_i8 v[2:5], v[10:13], v[240:243], v[2:5]
	v_mfma_i32_16x16x64_i8 v[26:29], v[18:21], v[226:229], v[22:25]
	v_mfma_i32_16x16x64_i8 v[22:25], v[30:33], v[222:225], v[166:169]
	v_mfma_i32_16x16x64_i8 v[10:13], v[18:21], v[248:251], v[2:5]
	v_mfma_i32_16x16x64_i8 v[2:5], v[30:33], v[240:243], v[6:9]
	v_mfma_i32_16x16x64_i8 v[22:25], v[62:65], v[226:229], v[22:25]
	v_mfma_i32_16x16x64_i8 v[6:9], v[62:65], v[248:251], v[2:5]
	s_setprio 0
	s_setprio 1
	v_mfma_i32_16x16x64_i8 v[2:5], v[198:201], v[34:37], v[14:17]
	v_mfma_i32_16x16x64_i8 v[62:65], v[202:205], v[46:49], v[2:5]
	v_mfma_i32_16x16x64_i8 v[2:5], v[206:209], v[34:37], v[170:173]
	v_mfma_i32_16x16x64_i8 v[50:53], v[210:213], v[46:49], v[2:5]
	v_mfma_i32_16x16x64_i8 v[2:5], v[198:201], v[214:217], v[174:177]
	v_mfma_i32_16x16x64_i8 v[46:49], v[202:205], v[218:221], v[2:5]
	v_mfma_i32_16x16x64_i8 v[2:5], v[206:209], v[214:217], v[178:181]
	v_mfma_i32_16x16x64_i8 v[34:37], v[210:213], v[218:221], v[2:5]
	v_mfma_i32_16x16x64_i8 v[2:5], v[198:201], v[222:225], v[182:185]
	v_mfma_i32_16x16x64_i8 v[30:33], v[202:205], v[226:229], v[2:5]
	v_mfma_i32_16x16x64_i8 v[2:5], v[206:209], v[222:225], v[186:189]
	v_mfma_i32_16x16x64_i8 v[18:21], v[210:213], v[226:229], v[2:5]
	v_mfma_i32_16x16x64_i8 v[2:5], v[198:201], v[240:243], v[190:193]
	v_mfma_i32_16x16x64_i8 v[14:17], v[202:205], v[248:251], v[2:5]
	v_mfma_i32_16x16x64_i8 v[2:5], v[206:209], v[240:243], v[194:197]
	v_mfma_i32_16x16x64_i8 v[2:5], v[210:213], v[248:251], v[2:5]
	s_setprio 0
	s_barrier
	s_add_u32 s34, s34, 0x20180
	s_addc_u32 s35, s35, 0
	s_add_u32 s74, s30, 0x200
	s_addc_u32 s54, s31, 0
	.p2align	6

.LBB0_1247:
	v_mov_b32_e32 v34, 0
	v_lshl_add_u64 v[176:177], v[2:3], 0, s[92:93]
	s_mov_b32 s70, -2
	v_mov_b32_e32 v35, v34
	v_mov_b32_e32 v36, v34
	v_mov_b32_e32 v37, v34
	v_mov_b32_e32 v38, v34
	v_mov_b32_e32 v39, v34
	v_mov_b32_e32 v40, v34
	v_mov_b32_e32 v41, v34
	v_mov_b32_e32 v50, v34
	v_mov_b32_e32 v51, v34
	v_mov_b32_e32 v52, v34
	v_mov_b32_e32 v53, v34
	v_mov_b32_e32 v54, v34
	v_mov_b32_e32 v55, v34
	v_mov_b32_e32 v56, v34
	v_mov_b32_e32 v57, v34
	v_mov_b32_e32 v66, v34
	v_mov_b32_e32 v67, v34
	v_mov_b32_e32 v68, v34
	v_mov_b32_e32 v69, v34
	v_mov_b32_e32 v70, v34
	v_mov_b32_e32 v71, v34
	v_mov_b32_e32 v72, v34
	v_mov_b32_e32 v73, v34
	v_mov_b32_e32 v82, v34
	v_mov_b32_e32 v83, v34
	v_mov_b32_e32 v84, v34
	v_mov_b32_e32 v85, v34
	v_mov_b32_e32 v86, v34
	v_mov_b32_e32 v87, v34
	v_mov_b32_e32 v88, v34
	v_mov_b32_e32 v89, v34
	v_mov_b32_e32 v42, v34
	v_mov_b32_e32 v43, v34
	v_mov_b32_e32 v44, v34
	v_mov_b32_e32 v45, v34
	v_mov_b32_e32 v46, v34
	v_mov_b32_e32 v47, v34
	v_mov_b32_e32 v48, v34
	v_mov_b32_e32 v49, v34
	v_mov_b32_e32 v58, v34
	v_mov_b32_e32 v59, v34
	v_mov_b32_e32 v60, v34
	v_mov_b32_e32 v61, v34
	v_mov_b32_e32 v62, v34
	v_mov_b32_e32 v63, v34
	v_mov_b32_e32 v64, v34
	v_mov_b32_e32 v65, v34
	v_mov_b32_e32 v74, v34
	v_mov_b32_e32 v75, v34
	v_mov_b32_e32 v76, v34
	v_mov_b32_e32 v77, v34
	v_mov_b32_e32 v78, v34
	v_mov_b32_e32 v79, v34
	v_mov_b32_e32 v80, v34
	v_mov_b32_e32 v81, v34
	v_mov_b32_e32 v90, v34
	v_mov_b32_e32 v91, v34
	v_mov_b32_e32 v92, v34
	v_mov_b32_e32 v93, v34
	v_mov_b32_e32 v94, v34
	v_mov_b32_e32 v95, v34
	v_mov_b32_e32 v96, v34
	v_mov_b32_e32 v97, v34
	v_mov_b32_e32 v98, v34
	v_mov_b32_e32 v99, v34
	v_mov_b32_e32 v100, v34
	v_mov_b32_e32 v101, v34
	v_mov_b32_e32 v102, v34
	v_mov_b32_e32 v103, v34
	v_mov_b32_e32 v104, v34
	v_mov_b32_e32 v105, v34
	v_mov_b32_e32 v114, v34
	v_mov_b32_e32 v115, v34
	v_mov_b32_e32 v116, v34
	v_mov_b32_e32 v117, v34
	v_mov_b32_e32 v118, v34
	v_mov_b32_e32 v119, v34
	v_mov_b32_e32 v120, v34
	v_mov_b32_e32 v121, v34
	v_mov_b32_e32 v130, v34
	v_mov_b32_e32 v131, v34
	v_mov_b32_e32 v132, v34
	v_mov_b32_e32 v133, v34
	v_mov_b32_e32 v134, v34
	v_mov_b32_e32 v135, v34
	v_mov_b32_e32 v136, v34
	v_mov_b32_e32 v137, v34
	v_mov_b32_e32 v146, v34
	v_mov_b32_e32 v147, v34
	v_mov_b32_e32 v148, v34
	v_mov_b32_e32 v149, v34
	v_mov_b32_e32 v150, v34
	v_mov_b32_e32 v151, v34
	v_mov_b32_e32 v152, v34
	v_mov_b32_e32 v153, v34
	v_mov_b32_e32 v106, v34
	v_mov_b32_e32 v107, v34
	v_mov_b32_e32 v108, v34
	v_mov_b32_e32 v109, v34
	v_mov_b32_e32 v110, v34
	v_mov_b32_e32 v111, v34
	v_mov_b32_e32 v112, v34
	v_mov_b32_e32 v113, v34
	v_mov_b32_e32 v122, v34
	v_mov_b32_e32 v123, v34
	v_mov_b32_e32 v124, v34
	v_mov_b32_e32 v125, v34
	v_mov_b32_e32 v126, v34
	v_mov_b32_e32 v127, v34
	v_mov_b32_e32 v128, v34
	v_mov_b32_e32 v129, v34
	v_mov_b32_e32 v138, v34
	v_mov_b32_e32 v139, v34
	v_mov_b32_e32 v140, v34
	v_mov_b32_e32 v141, v34
	v_mov_b32_e32 v142, v34
	v_mov_b32_e32 v143, v34
	v_mov_b32_e32 v144, v34
	v_mov_b32_e32 v145, v34
	v_mov_b32_e32 v154, v34
	v_mov_b32_e32 v155, v34
	v_mov_b32_e32 v156, v34
	v_mov_b32_e32 v157, v34
	v_mov_b32_e32 v158, v34
	v_mov_b32_e32 v159, v34
	v_mov_b32_e32 v160, v34
	v_mov_b32_e32 v161, v34
	.p2align	6

.LBB0_1293:
	v_lshl_add_u64 v[144:145], v[2:3], 0, s[92:93]
	v_mov_b32_e32 v2, 0
	s_mov_b32 s63, -2
	v_mov_b32_e32 v3, v2
	v_mov_b32_e32 v4, v2
	v_mov_b32_e32 v5, v2
	v_mov_b32_e32 v6, v2
	v_mov_b32_e32 v7, v2
	v_mov_b32_e32 v8, v2
	v_mov_b32_e32 v9, v2
	v_mov_b32_e32 v18, v2
	v_mov_b32_e32 v19, v2
	v_mov_b32_e32 v20, v2
	v_mov_b32_e32 v21, v2
	v_mov_b32_e32 v22, v2
	v_mov_b32_e32 v23, v2
	v_mov_b32_e32 v24, v2
	v_mov_b32_e32 v25, v2
	v_mov_b32_e32 v34, v2
	v_mov_b32_e32 v35, v2
	v_mov_b32_e32 v36, v2
	v_mov_b32_e32 v37, v2
	v_mov_b32_e32 v38, v2
	v_mov_b32_e32 v39, v2
	v_mov_b32_e32 v40, v2
	v_mov_b32_e32 v41, v2
	v_mov_b32_e32 v50, v2
	v_mov_b32_e32 v51, v2
	v_mov_b32_e32 v52, v2
	v_mov_b32_e32 v53, v2
	v_mov_b32_e32 v54, v2
	v_mov_b32_e32 v55, v2
	v_mov_b32_e32 v56, v2
	v_mov_b32_e32 v57, v2
	v_mov_b32_e32 v10, v2
	v_mov_b32_e32 v11, v2
	v_mov_b32_e32 v12, v2
	v_mov_b32_e32 v13, v2
	v_mov_b32_e32 v14, v2
	v_mov_b32_e32 v15, v2
	v_mov_b32_e32 v16, v2
	v_mov_b32_e32 v17, v2
	v_mov_b32_e32 v26, v2
	v_mov_b32_e32 v27, v2
	v_mov_b32_e32 v28, v2
	v_mov_b32_e32 v29, v2
	v_mov_b32_e32 v30, v2
	v_mov_b32_e32 v31, v2
	v_mov_b32_e32 v32, v2
	v_mov_b32_e32 v33, v2
	v_mov_b32_e32 v42, v2
	v_mov_b32_e32 v43, v2
	v_mov_b32_e32 v44, v2
	v_mov_b32_e32 v45, v2
	v_mov_b32_e32 v46, v2
	v_mov_b32_e32 v47, v2
	v_mov_b32_e32 v48, v2
	v_mov_b32_e32 v49, v2
	v_mov_b32_e32 v58, v2
	v_mov_b32_e32 v59, v2
	v_mov_b32_e32 v60, v2
	v_mov_b32_e32 v61, v2
	v_mov_b32_e32 v62, v2
	v_mov_b32_e32 v63, v2
	v_mov_b32_e32 v64, v2
	v_mov_b32_e32 v65, v2
	v_mov_b32_e32 v66, v2
	v_mov_b32_e32 v67, v2
	v_mov_b32_e32 v68, v2
	v_mov_b32_e32 v69, v2
	v_mov_b32_e32 v70, v2
	v_mov_b32_e32 v71, v2
	v_mov_b32_e32 v72, v2
	v_mov_b32_e32 v73, v2
	v_mov_b32_e32 v82, v2
	v_mov_b32_e32 v83, v2
	v_mov_b32_e32 v84, v2
	v_mov_b32_e32 v85, v2
	v_mov_b32_e32 v86, v2
	v_mov_b32_e32 v87, v2
	v_mov_b32_e32 v88, v2
	v_mov_b32_e32 v89, v2
	v_mov_b32_e32 v98, v2
	v_mov_b32_e32 v99, v2
	v_mov_b32_e32 v100, v2
	v_mov_b32_e32 v101, v2
	v_mov_b32_e32 v102, v2
	v_mov_b32_e32 v103, v2
	v_mov_b32_e32 v104, v2
	v_mov_b32_e32 v105, v2
	v_mov_b32_e32 v114, v2
	v_mov_b32_e32 v115, v2
	v_mov_b32_e32 v116, v2
	v_mov_b32_e32 v117, v2
	v_mov_b32_e32 v118, v2
	v_mov_b32_e32 v119, v2
	v_mov_b32_e32 v120, v2
	v_mov_b32_e32 v121, v2
	v_mov_b32_e32 v74, v2
	v_mov_b32_e32 v75, v2
	v_mov_b32_e32 v76, v2
	v_mov_b32_e32 v77, v2
	v_mov_b32_e32 v78, v2
	v_mov_b32_e32 v79, v2
	v_mov_b32_e32 v80, v2
	v_mov_b32_e32 v81, v2
	v_mov_b32_e32 v90, v2
	v_mov_b32_e32 v91, v2
	v_mov_b32_e32 v92, v2
	v_mov_b32_e32 v93, v2
	v_mov_b32_e32 v94, v2
	v_mov_b32_e32 v95, v2
	v_mov_b32_e32 v96, v2
	v_mov_b32_e32 v97, v2
	v_mov_b32_e32 v106, v2
	v_mov_b32_e32 v107, v2
	v_mov_b32_e32 v108, v2
	v_mov_b32_e32 v109, v2
	v_mov_b32_e32 v110, v2
	v_mov_b32_e32 v111, v2
	v_mov_b32_e32 v112, v2
	v_mov_b32_e32 v113, v2
	v_mov_b32_e32 v122, v2
	v_mov_b32_e32 v123, v2
	v_mov_b32_e32 v124, v2
	v_mov_b32_e32 v125, v2
	v_mov_b32_e32 v126, v2
	v_mov_b32_e32 v127, v2
	v_mov_b32_e32 v128, v2
	v_mov_b32_e32 v129, v2
	.p2align	6

.LBB0_1372:
	s_ashr_i32 s21, s20, 31
	s_lshl_b64 s[4:5], s[20:21], 18
	s_add_u32 s22, s30, s4
	s_addc_u32 s23, s31, s5
	s_and_b64 s[4:5], s[8:9], exec
	s_cselect_b32 s21, s23, s27
	s_cselect_b32 s62, s22, s26
	s_ashr_i32 s19, s18, 31
	s_lshl_b64 s[4:5], s[18:19], 18
	s_add_u32 s24, s33, s4
	s_addc_u32 s25, s34, s5
	s_and_b64 s[4:5], s[8:9], exec
	s_cselect_b32 s19, s25, s11
	s_cselect_b32 s63, s24, s10
	s_add_i32 s50, 0, 0x10000
	s_add_i32 s71, 0, 0x14000
	v_add_u32_e32 v140, s50, v144
	v_add_u32_e32 v141, s71, v144
	ds_read_b128 v[2:5], v140
	ds_read_b128 v[6:9], v140 offset:1024
	ds_read_b128 v[10:13], v140 offset:2048
	ds_read_b128 v[14:17], v140 offset:3072
	ds_read_b128 v[18:21], v141
	ds_read_b128 v[22:25], v141 offset:1024
	ds_read_b128 v[26:29], v141 offset:2048
	ds_read_b128 v[30:33], v141 offset:3072
	s_add_u32 s4, s26, 0x20080
	s_addc_u32 s5, s27, 0
	s_add_i32 s70, s36, 0xc000
	v_lshl_add_u64 v[66:67], s[4:5], 0, v[134:135]
	s_mov_b32 m0, s70
	ds_read_b128 v[34:37], v145
	ds_read_b128 v[38:41], v145 offset:1024
	ds_read_b128 v[42:45], v145 offset:2048
	ds_read_b128 v[46:49], v145 offset:3072
	ds_read_b128 v[50:53], v145 offset:4096
	ds_read_b128 v[54:57], v145 offset:5120
	ds_read_b128 v[58:61], v145 offset:6144
	ds_read_b128 v[62:65], v145 offset:7168
	global_load_lds_dwordx4 v[66:67], off
	v_lshl_add_u64 v[66:67], s[4:5], 0, v[132:133]
	s_add_i32 s4, s36, 0xe000
	s_mov_b32 m0, s4
	s_nop 0
	global_load_lds_dwordx4 v[66:67], off
	s_waitcnt vmcnt(8)
	s_waitcnt lgkmcnt(0)
	s_barrier
	s_setprio 1
	s_waitcnt lgkmcnt(0)
	v_mfma_i32_16x16x64_i8 v[90:93], v[2:5], v[58:61], 0
	s_mov_b32 s5, 0
	v_mfma_i32_16x16x64_i8 v[66:69], v[2:5], v[34:37], 0
	v_mfma_i32_16x16x64_i8 v[70:73], v[10:13], v[34:37], 0
	v_mfma_i32_16x16x64_i8 v[74:77], v[2:5], v[42:45], 0
	v_mfma_i32_16x16x64_i8 v[78:81], v[10:13], v[42:45], 0
	v_mfma_i32_16x16x64_i8 v[82:85], v[2:5], v[50:53], 0
	v_mfma_i32_16x16x64_i8 v[86:89], v[10:13], v[50:53], 0
	v_mfma_i32_16x16x64_i8 v[94:97], v[6:9], v[62:65], v[90:93]
	v_mfma_i32_16x16x64_i8 v[90:93], v[10:13], v[58:61], 0
	v_mfma_i32_16x16x64_i8 v[66:69], v[6:9], v[38:41], v[66:69]
	v_mfma_i32_16x16x64_i8 v[70:73], v[14:17], v[38:41], v[70:73]
	v_mfma_i32_16x16x64_i8 v[74:77], v[6:9], v[46:49], v[74:77]
	v_mfma_i32_16x16x64_i8 v[78:81], v[14:17], v[46:49], v[78:81]
	v_mfma_i32_16x16x64_i8 v[82:85], v[6:9], v[54:57], v[82:85]
	v_mfma_i32_16x16x64_i8 v[86:89], v[14:17], v[54:57], v[86:89]
	v_mfma_i32_16x16x64_i8 v[98:101], v[14:17], v[62:65], v[90:93]
	s_setprio 0
	s_setprio 1
	v_mfma_i32_16x16x64_i8 v[90:93], v[18:21], v[34:37], 0
	v_mfma_i32_16x16x64_i8 v[34:37], v[26:29], v[34:37], 0
	v_mfma_i32_16x16x64_i8 v[110:113], v[22:25], v[38:41], v[90:93]
	v_mfma_i32_16x16x64_i8 v[34:37], v[30:33], v[38:41], v[34:37]
	v_mfma_i32_16x16x64_i8 v[38:41], v[18:21], v[42:45], 0
	v_mfma_i32_16x16x64_i8 v[42:45], v[26:29], v[42:45], 0
	v_mfma_i32_16x16x64_i8 v[38:41], v[22:25], v[46:49], v[38:41]
	v_mfma_i32_16x16x64_i8 v[42:45], v[30:33], v[46:49], v[42:45]
	v_mfma_i32_16x16x64_i8 v[46:49], v[18:21], v[50:53], 0
	v_mfma_i32_16x16x64_i8 v[50:53], v[26:29], v[50:53], 0
	v_mfma_i32_16x16x64_i8 v[46:49], v[22:25], v[54:57], v[46:49]
	v_mfma_i32_16x16x64_i8 v[50:53], v[30:33], v[54:57], v[50:53]
	v_mfma_i32_16x16x64_i8 v[54:57], v[18:21], v[58:61], 0
	v_mfma_i32_16x16x64_i8 v[58:61], v[26:29], v[58:61], 0
	v_mfma_i32_16x16x64_i8 v[54:57], v[22:25], v[62:65], v[54:57]
	v_mfma_i32_16x16x64_i8 v[58:61], v[30:33], v[62:65], v[58:61]
	s_setprio 0
	s_barrier
	s_add_i32 s50, s50, s35
	v_lshl_add_u64 v[230:231], s[10:11], 0, v[0:1]
	s_add_i32 s51, s50, 0x2000
	v_lshl_add_u64 v[142:143], v[230:231], 0, s[92:93]
	s_mov_b32 m0, s50
	v_lshl_add_u64 v[232:233], s[10:11], 0, v[130:131]
	s_add_u32 s28, s10, 0x20100
	ds_read_b128 v[62:65], v145 offset:16384
	ds_read_b128 v[90:93], v145 offset:17408
	ds_read_b128 v[102:105], v145 offset:18432
	ds_read_b128 v[106:109], v145 offset:19456
	ds_read_b128 v[114:117], v145 offset:20480
	ds_read_b128 v[118:121], v145 offset:21504
	ds_read_b128 v[122:125], v145 offset:22528
	ds_read_b128 v[126:129], v145 offset:23552
	global_load_lds_dwordx4 v[142:143], off
	v_lshl_add_u64 v[142:143], v[232:233], 0, s[92:93]
	s_mov_b32 m0, s51
	s_addc_u32 s29, s11, 0
	s_add_i32 s71, s71, s35
	global_load_lds_dwordx4 v[142:143], off
	v_lshl_add_u64 v[142:143], s[28:29], 0, v[0:1]
	s_mov_b32 m0, s71
	s_add_i32 s75, s71, 0x2000
	global_load_lds_dwordx4 v[142:143], off
	v_lshl_add_u64 v[142:143], s[28:29], 0, v[130:131]
	s_mov_b32 m0, s75
	v_lshl_add_u64 v[244:245], s[26:27], 0, v[134:135]
	global_load_lds_dwordx4 v[142:143], off
	v_lshl_add_u64 v[142:143], v[244:245], 0, s[92:93]
	s_mov_b32 m0, s36
	v_lshl_add_u64 v[246:247], s[26:27], 0, v[132:133]
	global_load_lds_dwordx4 v[142:143], off
	v_lshl_add_u64 v[142:143], v[246:247], 0, s[92:93]
	s_mov_b32 m0, s37
	s_nop 0
	global_load_lds_dwordx4 v[142:143], off
	s_waitcnt vmcnt(8)
	s_waitcnt lgkmcnt(0)
	s_barrier
	s_setprio 1
	s_waitcnt lgkmcnt(0)
	v_mfma_i32_16x16x64_i8 v[146:149], v[2:5], v[62:65], 0
	v_mfma_i32_16x16x64_i8 v[154:157], v[2:5], v[102:105], 0
	v_mfma_i32_16x16x64_i8 v[162:165], v[2:5], v[114:117], 0
	v_mfma_i32_16x16x64_i8 v[2:5], v[2:5], v[122:125], 0
	v_mfma_i32_16x16x64_i8 v[146:149], v[6:9], v[90:93], v[146:149]
	v_mfma_i32_16x16x64_i8 v[154:157], v[6:9], v[106:109], v[154:157]
	v_mfma_i32_16x16x64_i8 v[162:165], v[6:9], v[118:121], v[162:165]
	v_mfma_i32_16x16x64_i8 v[2:5], v[6:9], v[126:129], v[2:5]
	v_mfma_i32_16x16x64_i8 v[6:9], v[10:13], v[122:125], 0
	v_mfma_i32_16x16x64_i8 v[150:153], v[10:13], v[62:65], 0
	v_mfma_i32_16x16x64_i8 v[158:161], v[10:13], v[102:105], 0
	v_mfma_i32_16x16x64_i8 v[166:169], v[10:13], v[114:117], 0
	v_mfma_i32_16x16x64_i8 v[6:9], v[14:17], v[126:129], v[6:9]
	v_mfma_i32_16x16x64_i8 v[150:153], v[14:17], v[90:93], v[150:153]
	v_mfma_i32_16x16x64_i8 v[158:161], v[14:17], v[106:109], v[158:161]
	v_mfma_i32_16x16x64_i8 v[166:169], v[14:17], v[118:121], v[166:169]
	s_setprio 0
	s_setprio 1
	v_mfma_i32_16x16x64_i8 v[10:13], v[18:21], v[62:65], 0
	v_mfma_i32_16x16x64_i8 v[14:17], v[22:25], v[90:93], v[10:13]
	v_mfma_i32_16x16x64_i8 v[10:13], v[26:29], v[62:65], 0
	v_mfma_i32_16x16x64_i8 v[170:173], v[30:33], v[90:93], v[10:13]
	v_mfma_i32_16x16x64_i8 v[10:13], v[18:21], v[102:105], 0
	v_mfma_i32_16x16x64_i8 v[174:177], v[22:25], v[106:109], v[10:13]
	v_mfma_i32_16x16x64_i8 v[10:13], v[26:29], v[102:105], 0
	v_mfma_i32_16x16x64_i8 v[178:181], v[30:33], v[106:109], v[10:13]
	v_mfma_i32_16x16x64_i8 v[10:13], v[18:21], v[114:117], 0
	v_mfma_i32_16x16x64_i8 v[182:185], v[22:25], v[118:121], v[10:13]
	v_mfma_i32_16x16x64_i8 v[10:13], v[26:29], v[114:117], 0
	v_mfma_i32_16x16x64_i8 v[186:189], v[30:33], v[118:121], v[10:13]
	v_mfma_i32_16x16x64_i8 v[10:13], v[18:21], v[122:125], 0
	v_mfma_i32_16x16x64_i8 v[190:193], v[22:25], v[126:129], v[10:13]
	v_mfma_i32_16x16x64_i8 v[10:13], v[26:29], v[122:125], 0
	v_mfma_i32_16x16x64_i8 v[194:197], v[30:33], v[126:129], v[10:13]
	s_setprio 0
	s_barrier
	s_add_i32 s78, 0, 0x18000
	s_add_i32 s58, 0, 0x1c000
	v_add_u32_e32 v142, s78, v144
	v_add_u32_e32 v143, s58, v144
	s_nop 0
	ds_read_b128 v[10:13], v142
	ds_read_b128 v[18:21], v142 offset:1024
	ds_read_b128 v[30:33], v142 offset:2048
	ds_read_b128 v[62:65], v142 offset:3072
	ds_read_b128 v[198:201], v143
	ds_read_b128 v[202:205], v143 offset:1024
	ds_read_b128 v[206:209], v143 offset:2048
	ds_read_b128 v[210:213], v143 offset:3072
	s_add_u32 s28, s26, 0x20100
	s_addc_u32 s29, s27, 0
	s_mov_b32 m0, s38
	v_lshl_add_u64 v[90:91], s[28:29], 0, v[134:135]
	ds_read_b128 v[22:25], v145 offset:32768
	ds_read_b128 v[26:29], v145 offset:33792
	ds_read_b128 v[214:217], v145 offset:34816
	ds_read_b128 v[218:221], v145 offset:35840
	ds_read_b128 v[222:225], v145 offset:36864
	ds_read_b128 v[226:229], v145 offset:37888
	ds_read_b128 v[240:243], v145 offset:38912
	ds_read_b128 v[248:251], v145 offset:39936
	global_load_lds_dwordx4 v[90:91], off
	v_lshl_add_u64 v[90:91], s[28:29], 0, v[132:133]
	s_mov_b32 m0, s39
	s_nop 0
	global_load_lds_dwordx4 v[90:91], off
	s_waitcnt vmcnt(8)
	s_waitcnt lgkmcnt(0)
	s_barrier
	s_setprio 1
	s_waitcnt lgkmcnt(0)
	v_mfma_i32_16x16x64_i8 v[66:69], v[10:13], v[22:25], v[66:69]
	v_mfma_i32_16x16x64_i8 v[122:125], v[18:21], v[26:29], v[66:69]
	v_mfma_i32_16x16x64_i8 v[66:69], v[30:33], v[22:25], v[70:73]
	v_mfma_i32_16x16x64_i8 v[118:121], v[62:65], v[26:29], v[66:69]
	v_mfma_i32_16x16x64_i8 v[66:69], v[10:13], v[214:217], v[74:77]
	v_mfma_i32_16x16x64_i8 v[106:109], v[18:21], v[218:221], v[66:69]
	v_mfma_i32_16x16x64_i8 v[66:69], v[30:33], v[214:217], v[78:81]
	v_mfma_i32_16x16x64_i8 v[102:105], v[62:65], v[218:221], v[66:69]
	v_mfma_i32_16x16x64_i8 v[66:69], v[10:13], v[222:225], v[82:85]
	v_mfma_i32_16x16x64_i8 v[90:93], v[18:21], v[226:229], v[66:69]
	v_mfma_i32_16x16x64_i8 v[66:69], v[30:33], v[222:225], v[86:89]
	v_mfma_i32_16x16x64_i8 v[86:89], v[62:65], v[226:229], v[66:69]
	v_mfma_i32_16x16x64_i8 v[66:69], v[10:13], v[240:243], v[94:97]
	v_mfma_i32_16x16x64_i8 v[74:77], v[18:21], v[248:251], v[66:69]
	v_mfma_i32_16x16x64_i8 v[66:69], v[30:33], v[240:243], v[98:101]
	v_mfma_i32_16x16x64_i8 v[70:73], v[62:65], v[248:251], v[66:69]
	s_setprio 0
	s_setprio 1
	v_mfma_i32_16x16x64_i8 v[66:69], v[198:201], v[22:25], v[110:113]
	v_mfma_i32_16x16x64_i8 v[22:25], v[206:209], v[22:25], v[34:37]
	v_mfma_i32_16x16x64_i8 v[114:117], v[210:213], v[26:29], v[22:25]
	v_mfma_i32_16x16x64_i8 v[22:25], v[198:201], v[214:217], v[38:41]
	v_mfma_i32_16x16x64_i8 v[110:113], v[202:205], v[218:221], v[22:25]
	v_mfma_i32_16x16x64_i8 v[22:25], v[206:209], v[214:217], v[42:45]
	v_mfma_i32_16x16x64_i8 v[98:101], v[210:213], v[218:221], v[22:25]
	v_mfma_i32_16x16x64_i8 v[22:25], v[198:201], v[222:225], v[46:49]
	v_mfma_i32_16x16x64_i8 v[94:97], v[202:205], v[226:229], v[22:25]
	v_mfma_i32_16x16x64_i8 v[22:25], v[206:209], v[222:225], v[50:53]
	v_mfma_i32_16x16x64_i8 v[82:85], v[210:213], v[226:229], v[22:25]
	v_mfma_i32_16x16x64_i8 v[22:25], v[198:201], v[240:243], v[54:57]
	v_mfma_i32_16x16x64_i8 v[78:81], v[202:205], v[248:251], v[22:25]
	v_mfma_i32_16x16x64_i8 v[22:25], v[206:209], v[240:243], v[58:61]
	v_mfma_i32_16x16x64_i8 v[126:129], v[202:205], v[26:29], v[66:69]
	v_mfma_i32_16x16x64_i8 v[66:69], v[210:213], v[248:251], v[22:25]
	s_setprio 0
	s_barrier
	s_add_i32 s78, s78, s35
	s_mov_b64 s[54:55], 0x180
	s_add_i32 s79, s78, 0x2000
	s_nop 0
	v_lshl_add_u64 v[22:23], v[230:231], 0, s[54:55]
	s_mov_b32 m0, s78
	s_add_u32 s28, s10, 0x20180
	ds_read_b128 v[34:37], v145 offset:49152
	ds_read_b128 v[46:49], v145 offset:50176
	ds_read_b128 v[214:217], v145 offset:51200
	ds_read_b128 v[218:221], v145 offset:52224
	ds_read_b128 v[222:225], v145 offset:53248
	ds_read_b128 v[226:229], v145 offset:54272
	ds_read_b128 v[240:243], v145 offset:55296
	ds_read_b128 v[248:251], v145 offset:56320
	global_load_lds_dwordx4 v[22:23], off
	v_lshl_add_u64 v[22:23], v[232:233], 0, s[54:55]
	s_mov_b32 m0, s79
	s_addc_u32 s29, s11, 0
	s_add_i32 s58, s58, s35
	global_load_lds_dwordx4 v[22:23], off
	v_lshl_add_u64 v[22:23], s[28:29], 0, v[0:1]
	s_mov_b32 m0, s58
	s_add_i32 s48, s58, 0x2000
	global_load_lds_dwordx4 v[22:23], off
	v_lshl_add_u64 v[22:23], s[28:29], 0, v[130:131]
	s_mov_b32 m0, s48
	s_nop 0
	global_load_lds_dwordx4 v[22:23], off
	v_lshl_add_u64 v[22:23], v[244:245], 0, s[54:55]
	s_mov_b32 m0, s45
	s_nop 0
	global_load_lds_dwordx4 v[22:23], off
	v_lshl_add_u64 v[22:23], v[246:247], 0, s[54:55]
	s_mov_b32 m0, s49
	s_nop 0
	global_load_lds_dwordx4 v[22:23], off
	s_waitcnt vmcnt(8)
	s_waitcnt lgkmcnt(0)
	s_barrier
	s_setprio 1
	s_waitcnt lgkmcnt(0)
	v_mfma_i32_16x16x64_i8 v[22:25], v[10:13], v[34:37], v[146:149]
	v_mfma_i32_16x16x64_i8 v[58:61], v[18:21], v[46:49], v[22:25]
	v_mfma_i32_16x16x64_i8 v[22:25], v[30:33], v[34:37], v[150:153]
	v_mfma_i32_16x16x64_i8 v[54:57], v[62:65], v[46:49], v[22:25]
	v_mfma_i32_16x16x64_i8 v[22:25], v[10:13], v[214:217], v[154:157]
	v_mfma_i32_16x16x64_i8 v[42:45], v[18:21], v[218:221], v[22:25]
	v_mfma_i32_16x16x64_i8 v[22:25], v[30:33], v[214:217], v[158:161]
	v_mfma_i32_16x16x64_i8 v[38:41], v[62:65], v[218:221], v[22:25]
	v_mfma_i32_16x16x64_i8 v[22:25], v[10:13], v[222:225], v[162:165]
	v_mfma_i32_16x16x64_i8 v[2:5], v[10:13], v[240:243], v[2:5]
	v_mfma_i32_16x16x64_i8 v[26:29], v[18:21], v[226:229], v[22:25]
	v_mfma_i32_16x16x64_i8 v[22:25], v[30:33], v[222:225], v[166:169]
	v_mfma_i32_16x16x64_i8 v[10:13], v[18:21], v[248:251], v[2:5]
	v_mfma_i32_16x16x64_i8 v[2:5], v[30:33], v[240:243], v[6:9]
	v_mfma_i32_16x16x64_i8 v[22:25], v[62:65], v[226:229], v[22:25]
	v_mfma_i32_16x16x64_i8 v[6:9], v[62:65], v[248:251], v[2:5]
	s_setprio 0
	s_setprio 1
	v_mfma_i32_16x16x64_i8 v[2:5], v[198:201], v[34:37], v[14:17]
	v_mfma_i32_16x16x64_i8 v[62:65], v[202:205], v[46:49], v[2:5]
	v_mfma_i32_16x16x64_i8 v[2:5], v[206:209], v[34:37], v[170:173]
	v_mfma_i32_16x16x64_i8 v[50:53], v[210:213], v[46:49], v[2:5]
	v_mfma_i32_16x16x64_i8 v[2:5], v[198:201], v[214:217], v[174:177]
	v_mfma_i32_16x16x64_i8 v[46:49], v[202:205], v[218:221], v[2:5]
	v_mfma_i32_16x16x64_i8 v[2:5], v[206:209], v[214:217], v[178:181]
	v_mfma_i32_16x16x64_i8 v[34:37], v[210:213], v[218:221], v[2:5]
	v_mfma_i32_16x16x64_i8 v[2:5], v[198:201], v[222:225], v[182:185]
	v_mfma_i32_16x16x64_i8 v[30:33], v[202:205], v[226:229], v[2:5]
	v_mfma_i32_16x16x64_i8 v[2:5], v[206:209], v[222:225], v[186:189]
	v_mfma_i32_16x16x64_i8 v[18:21], v[210:213], v[226:229], v[2:5]
	v_mfma_i32_16x16x64_i8 v[2:5], v[198:201], v[240:243], v[190:193]
	v_mfma_i32_16x16x64_i8 v[14:17], v[202:205], v[248:251], v[2:5]
	v_mfma_i32_16x16x64_i8 v[2:5], v[206:209], v[240:243], v[194:197]
	v_mfma_i32_16x16x64_i8 v[2:5], v[210:213], v[248:251], v[2:5]
	s_setprio 0
	s_barrier
	s_add_u32 s26, s26, 0x20180
	s_addc_u32 s27, s27, 0
	s_add_u32 s80, s10, 0x200
	s_addc_u32 s74, s11, 0
	.p2align	6

.LBB0_1474:
	s_add_u32 s45, s18, 0x100
	v_mov_b32_e32 v34, 0
	s_addc_u32 s49, s19, 0
	s_mov_b32 s52, -2
	v_mov_b32_e32 v35, v34
	v_mov_b32_e32 v36, v34
	v_mov_b32_e32 v37, v34
	v_mov_b32_e32 v38, v34
	v_mov_b32_e32 v39, v34
	v_mov_b32_e32 v40, v34
	v_mov_b32_e32 v41, v34
	v_mov_b32_e32 v46, v34
	v_mov_b32_e32 v47, v34
	v_mov_b32_e32 v48, v34
	v_mov_b32_e32 v49, v34
	v_mov_b32_e32 v54, v34
	v_mov_b32_e32 v55, v34
	v_mov_b32_e32 v56, v34
	v_mov_b32_e32 v57, v34
	v_mov_b32_e32 v62, v34
	v_mov_b32_e32 v63, v34
	v_mov_b32_e32 v64, v34
	v_mov_b32_e32 v65, v34
	v_mov_b32_e32 v70, v34
	v_mov_b32_e32 v71, v34
	v_mov_b32_e32 v72, v34
	v_mov_b32_e32 v73, v34
	v_mov_b32_e32 v78, v34
	v_mov_b32_e32 v79, v34
	v_mov_b32_e32 v80, v34
	v_mov_b32_e32 v81, v34
	v_mov_b32_e32 v86, v34
	v_mov_b32_e32 v87, v34
	v_mov_b32_e32 v88, v34
	v_mov_b32_e32 v89, v34
	v_mov_b32_e32 v42, v34
	v_mov_b32_e32 v43, v34
	v_mov_b32_e32 v44, v34
	v_mov_b32_e32 v45, v34
	v_mov_b32_e32 v50, v34
	v_mov_b32_e32 v51, v34
	v_mov_b32_e32 v52, v34
	v_mov_b32_e32 v53, v34
	v_mov_b32_e32 v58, v34
	v_mov_b32_e32 v59, v34
	v_mov_b32_e32 v60, v34
	v_mov_b32_e32 v61, v34
	v_mov_b32_e32 v66, v34
	v_mov_b32_e32 v67, v34
	v_mov_b32_e32 v68, v34
	v_mov_b32_e32 v69, v34
	v_mov_b32_e32 v74, v34
	v_mov_b32_e32 v75, v34
	v_mov_b32_e32 v76, v34
	v_mov_b32_e32 v77, v34
	v_mov_b32_e32 v82, v34
	v_mov_b32_e32 v83, v34
	v_mov_b32_e32 v84, v34
	v_mov_b32_e32 v85, v34
	v_mov_b32_e32 v90, v34
	v_mov_b32_e32 v91, v34
	v_mov_b32_e32 v92, v34
	v_mov_b32_e32 v93, v34
	v_mov_b32_e32 v94, v34
	v_mov_b32_e32 v95, v34
	v_mov_b32_e32 v96, v34
	v_mov_b32_e32 v97, v34
	v_mov_b32_e32 v98, v34
	v_mov_b32_e32 v99, v34
	v_mov_b32_e32 v100, v34
	v_mov_b32_e32 v101, v34
	v_mov_b32_e32 v102, v34
	v_mov_b32_e32 v103, v34
	v_mov_b32_e32 v104, v34
	v_mov_b32_e32 v105, v34
	v_mov_b32_e32 v106, v34
	v_mov_b32_e32 v107, v34
	v_mov_b32_e32 v108, v34
	v_mov_b32_e32 v109, v34
	v_mov_b32_e32 v110, v34
	v_mov_b32_e32 v111, v34
	v_mov_b32_e32 v112, v34
	v_mov_b32_e32 v113, v34
	v_mov_b32_e32 v122, v34
	v_mov_b32_e32 v123, v34
	v_mov_b32_e32 v124, v34
	v_mov_b32_e32 v125, v34
	v_mov_b32_e32 v126, v34
	v_mov_b32_e32 v127, v34
	v_mov_b32_e32 v128, v34
	v_mov_b32_e32 v129, v34
	v_mov_b32_e32 v138, v34
	v_mov_b32_e32 v139, v34
	v_mov_b32_e32 v140, v34
	v_mov_b32_e32 v141, v34
	v_mov_b32_e32 v150, v34
	v_mov_b32_e32 v151, v34
	v_mov_b32_e32 v152, v34
	v_mov_b32_e32 v153, v34
	v_mov_b32_e32 v114, v34
	v_mov_b32_e32 v115, v34
	v_mov_b32_e32 v116, v34
	v_mov_b32_e32 v117, v34
	v_mov_b32_e32 v118, v34
	v_mov_b32_e32 v119, v34
	v_mov_b32_e32 v120, v34
	v_mov_b32_e32 v121, v34
	v_mov_b32_e32 v130, v34
	v_mov_b32_e32 v131, v34
	v_mov_b32_e32 v132, v34
	v_mov_b32_e32 v133, v34
	v_mov_b32_e32 v134, v34
	v_mov_b32_e32 v135, v34
	v_mov_b32_e32 v136, v34
	v_mov_b32_e32 v137, v34
	v_mov_b32_e32 v142, v34
	v_mov_b32_e32 v143, v34
	v_mov_b32_e32 v144, v34
	v_mov_b32_e32 v145, v34
	v_mov_b32_e32 v146, v34
	v_mov_b32_e32 v147, v34
	v_mov_b32_e32 v148, v34
	v_mov_b32_e32 v149, v34
	v_mov_b32_e32 v154, v34
	v_mov_b32_e32 v155, v34
	v_mov_b32_e32 v156, v34
	v_mov_b32_e32 v157, v34
	v_mov_b32_e32 v158, v34
	v_mov_b32_e32 v159, v34
	v_mov_b32_e32 v160, v34
	v_mov_b32_e32 v161, v34
	.p2align	6

.LBB0_1500:
	s_add_u32 s45, s20, 0x100
	v_mov_b32_e32 v2, 0
	s_addc_u32 s49, s21, 0
	s_mov_b32 s52, -2
	v_mov_b32_e32 v3, v2
	v_mov_b32_e32 v4, v2
	v_mov_b32_e32 v5, v2
	v_mov_b32_e32 v6, v2
	v_mov_b32_e32 v7, v2
	v_mov_b32_e32 v8, v2
	v_mov_b32_e32 v9, v2
	v_mov_b32_e32 v14, v2
	v_mov_b32_e32 v15, v2
	v_mov_b32_e32 v16, v2
	v_mov_b32_e32 v17, v2
	v_mov_b32_e32 v22, v2
	v_mov_b32_e32 v23, v2
	v_mov_b32_e32 v24, v2
	v_mov_b32_e32 v25, v2
	v_mov_b32_e32 v30, v2
	v_mov_b32_e32 v31, v2
	v_mov_b32_e32 v32, v2
	v_mov_b32_e32 v33, v2
	v_mov_b32_e32 v38, v2
	v_mov_b32_e32 v39, v2
	v_mov_b32_e32 v40, v2
	v_mov_b32_e32 v41, v2
	v_mov_b32_e32 v46, v2
	v_mov_b32_e32 v47, v2
	v_mov_b32_e32 v48, v2
	v_mov_b32_e32 v49, v2
	v_mov_b32_e32 v54, v2
	v_mov_b32_e32 v55, v2
	v_mov_b32_e32 v56, v2
	v_mov_b32_e32 v57, v2
	v_mov_b32_e32 v10, v2
	v_mov_b32_e32 v11, v2
	v_mov_b32_e32 v12, v2
	v_mov_b32_e32 v13, v2
	v_mov_b32_e32 v18, v2
	v_mov_b32_e32 v19, v2
	v_mov_b32_e32 v20, v2
	v_mov_b32_e32 v21, v2
	v_mov_b32_e32 v26, v2
	v_mov_b32_e32 v27, v2
	v_mov_b32_e32 v28, v2
	v_mov_b32_e32 v29, v2
	v_mov_b32_e32 v34, v2
	v_mov_b32_e32 v35, v2
	v_mov_b32_e32 v36, v2
	v_mov_b32_e32 v37, v2
	v_mov_b32_e32 v42, v2
	v_mov_b32_e32 v43, v2
	v_mov_b32_e32 v44, v2
	v_mov_b32_e32 v45, v2
	v_mov_b32_e32 v50, v2
	v_mov_b32_e32 v51, v2
	v_mov_b32_e32 v52, v2
	v_mov_b32_e32 v53, v2
	v_mov_b32_e32 v58, v2
	v_mov_b32_e32 v59, v2
	v_mov_b32_e32 v60, v2
	v_mov_b32_e32 v61, v2
	v_mov_b32_e32 v62, v2
	v_mov_b32_e32 v63, v2
	v_mov_b32_e32 v64, v2
	v_mov_b32_e32 v65, v2
	v_mov_b32_e32 v66, v2
	v_mov_b32_e32 v67, v2
	v_mov_b32_e32 v68, v2
	v_mov_b32_e32 v69, v2
	v_mov_b32_e32 v70, v2
	v_mov_b32_e32 v71, v2
	v_mov_b32_e32 v72, v2
	v_mov_b32_e32 v73, v2
	v_mov_b32_e32 v74, v2
	v_mov_b32_e32 v75, v2
	v_mov_b32_e32 v76, v2
	v_mov_b32_e32 v77, v2
	v_mov_b32_e32 v78, v2
	v_mov_b32_e32 v79, v2
	v_mov_b32_e32 v80, v2
	v_mov_b32_e32 v81, v2
	v_mov_b32_e32 v90, v2
	v_mov_b32_e32 v91, v2
	v_mov_b32_e32 v92, v2
	v_mov_b32_e32 v93, v2
	v_mov_b32_e32 v94, v2
	v_mov_b32_e32 v95, v2
	v_mov_b32_e32 v96, v2
	v_mov_b32_e32 v97, v2
	v_mov_b32_e32 v106, v2
	v_mov_b32_e32 v107, v2
	v_mov_b32_e32 v108, v2
	v_mov_b32_e32 v109, v2
	v_mov_b32_e32 v118, v2
	v_mov_b32_e32 v119, v2
	v_mov_b32_e32 v120, v2
	v_mov_b32_e32 v121, v2
	v_mov_b32_e32 v82, v2
	v_mov_b32_e32 v83, v2
	v_mov_b32_e32 v84, v2
	v_mov_b32_e32 v85, v2
	v_mov_b32_e32 v86, v2
	v_mov_b32_e32 v87, v2
	v_mov_b32_e32 v88, v2
	v_mov_b32_e32 v89, v2
	v_mov_b32_e32 v98, v2
	v_mov_b32_e32 v99, v2
	v_mov_b32_e32 v100, v2
	v_mov_b32_e32 v101, v2
	v_mov_b32_e32 v102, v2
	v_mov_b32_e32 v103, v2
	v_mov_b32_e32 v104, v2
	v_mov_b32_e32 v105, v2
	v_mov_b32_e32 v110, v2
	v_mov_b32_e32 v111, v2
	v_mov_b32_e32 v112, v2
	v_mov_b32_e32 v113, v2
	v_mov_b32_e32 v114, v2
	v_mov_b32_e32 v115, v2
	v_mov_b32_e32 v116, v2
	v_mov_b32_e32 v117, v2
	v_mov_b32_e32 v122, v2
	v_mov_b32_e32 v123, v2
	v_mov_b32_e32 v124, v2
	v_mov_b32_e32 v125, v2
	v_mov_b32_e32 v126, v2
	v_mov_b32_e32 v127, v2
	v_mov_b32_e32 v128, v2
	v_mov_b32_e32 v129, v2
	.p2align	6
